# baseline (speedup 1.0000x reference)
_Z7gemm2_kILi0ELi3ELi1EEv5GArgs:
	v_lshlrev_b32_e32 v186, 4, v0
	s_getpc_b64 s[92:93]
	s_add_u32 s92, s92, 0xffff89f8
	s_addc_u32 s93, s93, 0xffffffff
	global_load_dword v187, v186, s[92:93]
	s_load_dwordx8 s[8:15], s[0:1], 0x68
	s_cmpk_lt_u32 s2, 0xc0
	s_mov_b64 s[4:5], -1
	s_cbranch_scc0 .LBB11_26
	v_lshrrev_b32_e32 v149, 6, v0
	s_lshl_b32 s3, s2, 8
	v_bfe_u32 v1, v0, 3, 3
	s_load_dwordx4 s[4:7], s[0:1], 0x0
	s_load_dwordx4 s[16:19], s[0:1], 0x18
	s_and_b32 s20, s3, 0xf00
	v_lshl_or_b32 v6, v149, 5, v1
	v_or_b32_e32 v8, s20, v6
	v_mul_u32_u24_e32 v2, 0x340, v8
	v_bfe_u32 v4, v0, 4, 2
	v_lshlrev_b32_e32 v146, 1, v2
	v_mov_b32_e32 v147, 0
	v_bitop3_b32 v4, v4, v0, 7 bitop3:0x78
	s_waitcnt lgkmcnt(0)
	v_lshl_add_u64 v[2:3], s[4:5], 0, v[146:147]
	v_lshlrev_b32_e32 v146, 4, v4
	v_or_b32_e32 v4, 8, v6
	v_lshl_add_u64 v[98:99], v[2:3], 0, v[146:147]
	v_or_b32_e32 v2, s20, v4
	v_lshrrev_b32_e32 v4, 1, v4
	v_xor_b32_e32 v4, v4, v0
	v_mul_u32_u24_e32 v2, 0x340, v2
	v_mov_b32_e32 v3, v147
	v_lshlrev_b32_e32 v4, 4, v4
	v_lshl_add_u64 v[2:3], v[2:3], 1, s[4:5]
	v_and_b32_e32 v4, 0x70, v4
	v_mov_b32_e32 v5, v147
	v_lshl_add_u64 v[100:101], v[2:3], 0, v[4:5]
	v_or_b32_e32 v2, 16, v8
	v_mul_u32_u24_e32 v2, 0x340, v2
	v_mov_b32_e32 v3, v147
	v_lshl_add_u64 v[2:3], v[2:3], 1, s[4:5]
	v_xor_b32_e32 v146, 16, v146
	v_or_b32_e32 v4, 24, v6
	v_lshl_add_u64 v[102:103], v[2:3], 0, v[146:147]
	v_or_b32_e32 v2, s20, v4
	v_lshrrev_b32_e32 v4, 1, v4
	v_xor_b32_e32 v4, v4, v0
	v_lshlrev_b32_e32 v4, 3, v4
	v_mul_u32_u24_e32 v146, 0x340, v2
	v_bitop3_b32 v4, v4, 8, 56 bitop3:0x6c
	s_lshr_b32 s36, s2, 6
	s_bfe_u32 s21, s2, 0x20004
	v_lshl_add_u64 v[2:3], v[146:147], 1, s[4:5]
	v_lshlrev_b32_e32 v146, 1, v4
	v_lshl_add_u64 v[104:105], v[2:3], 0, v[146:147]
	s_mul_i32 s20, s21, 0xc0
	s_mul_i32 s4, s36, 0x300
	v_mul_u32_u24_e32 v2, 24, v149
	v_mul_u32_u24_e32 v4, 3, v149
	s_add_i32 s21, s20, s4
	v_or_b32_e32 v5, v2, v1
	v_add_u32_e32 v2, s21, v5
	v_bfe_u32 v5, v5, 1, 3
	v_lshrrev_b32_e32 v4, 1, v4
	v_and_b32_e32 v7, 7, v0
	s_movk_i32 s22, 0x680
	v_bitop3_b32 v4, v4, v5, 1 bitop3:0x6c
	v_mad_u32_u24 v6, v149, 3, 1
	v_mul_lo_u32 v146, v2, s22
	v_xor_b32_e32 v4, v4, v7
	v_lshl_or_b32 v8, v6, 3, v1
	v_lshl_add_u64 v[2:3], s[6:7], 0, v[146:147]
	v_lshlrev_b32_e32 v146, 4, v4
	v_add_u32_e32 v4, s21, v8
	v_bfe_u32 v8, v8, 1, 3
	v_lshrrev_b32_e32 v9, 1, v6
	v_bitop3_b32 v8, v9, v8, 1 bitop3:0x6c
	v_lshl_add_u64 v[106:107], v[2:3], 0, v[146:147]
	v_mov_b64_e32 v[2:3], s[6:7]
	v_xor_b32_e32 v8, v8, v7
	v_mad_u64_u32 v[4:5], s[4:5], v4, s22, v[2:3]
	v_lshlrev_b32_e32 v146, 4, v8
	v_lshl_add_u64 v[108:109], v[4:5], 0, v[146:147]
	v_mad_u32_u24 v4, v149, 3, 2
	v_lshl_or_b32 v1, v4, 3, v1
	v_add_u32_e32 v5, s21, v1
	v_mad_u64_u32 v[2:3], s[4:5], v5, s22, v[2:3]
	v_bfe_u32 v1, v1, 1, 3
	v_lshrrev_b32_e32 v5, 1, v4
	v_lshlrev_b32_e32 v141, 12, v149
	v_bitop3_b32 v1, v5, v1, 1 bitop3:0x6c
	v_readfirstlane_b32 s33, v141
	v_or_b32_e32 v142, 0x400, v141
	v_xor_b32_e32 v1, v1, v7
	s_mov_b32 m0, s33
	v_readfirstlane_b32 s28, v142
	v_or_b32_e32 v143, 0x800, v141
	v_lshlrev_b32_e32 v146, 4, v1
	global_load_lds_dwordx4 v[98:99], off
	s_mov_b32 m0, s28
	v_readfirstlane_b32 s29, v143
	v_or_b32_e32 v144, 0xc00, v141
	v_mul_u32_u24_e32 v1, 0xc00, v149
	global_load_lds_dwordx4 v[100:101], off
	s_mov_b32 m0, s29
	v_readfirstlane_b32 s30, v144
	v_or_b32_e32 v145, 0x10000, v1
	v_lshlrev_b32_e32 v1, 10, v6
	v_lshl_add_u64 v[110:111], v[2:3], 0, v[146:147]
	global_load_lds_dwordx4 v[102:103], off
	s_mov_b32 m0, s30
	v_readfirstlane_b32 s31, v145
	v_or_b32_e32 v146, 0x10000, v1
	v_lshlrev_b32_e32 v4, 10, v4
	global_load_lds_dwordx4 v[104:105], off
	s_mov_b32 m0, s31
	v_readfirstlane_b32 s34, v146
	v_or_b32_e32 v148, 0x10000, v4
	global_load_lds_dwordx4 v[106:107], off
	s_mov_b32 m0, s34
	v_readfirstlane_b32 s35, v148
	v_or_b32_e32 v134, 0x8000, v141
	global_load_lds_dwordx4 v[108:109], off
	s_mov_b32 m0, s35
	s_mov_b64 s[4:5], 0x80
	v_readfirstlane_b32 s24, v134
	v_or_b32_e32 v135, 0x8400, v141
	global_load_lds_dwordx4 v[110:111], off
	v_lshl_add_u64 v[2:3], v[98:99], 0, s[4:5]
	s_mov_b32 m0, s24
	v_readfirstlane_b32 s21, v135
	v_or_b32_e32 v136, 0x8800, v141
	s_movk_i32 s6, 0xc00
	s_waitcnt vmcnt(0)
	s_waitcnt vmcnt(0) lgkmcnt(0)
	s_barrier
	global_load_lds_dwordx4 v[2:3], off
	v_lshl_add_u64 v[2:3], v[100:101], 0, s[4:5]
	s_mov_b32 m0, s21
	v_readfirstlane_b32 s22, v136
	v_or_b32_e32 v137, 0x8c00, v141
	v_mov_b32_e32 v5, 0x16000
	global_load_lds_dwordx4 v[2:3], off
	v_lshl_add_u64 v[2:3], v[102:103], 0, s[4:5]
	s_mov_b32 m0, s22
	v_readfirstlane_b32 s23, v137
	v_mad_u32_u24 v138, v149, s6, v5
	global_load_lds_dwordx4 v[2:3], off
	v_lshl_add_u64 v[2:3], v[104:105], 0, s[4:5]
	s_mov_b32 m0, s23
	v_readfirstlane_b32 s25, v138
	v_add_u32_e32 v139, 0x16000, v1
	global_load_lds_dwordx4 v[2:3], off
	v_lshl_add_u64 v[2:3], v[106:107], 0, s[4:5]
	s_mov_b32 m0, s25
	v_readfirstlane_b32 s26, v139
	v_add_u32_e32 v140, 0x16000, v4
	global_load_lds_dwordx4 v[2:3], off
	v_lshl_add_u64 v[2:3], v[108:109], 0, s[4:5]
	s_mov_b32 m0, s26
	v_readfirstlane_b32 s27, v140
	global_load_lds_dwordx4 v[2:3], off
	v_lshl_add_u64 v[2:3], v[110:111], 0, s[4:5]
	s_mov_b32 m0, s27
	v_and_b32_e32 v156, 31, v0
	global_load_lds_dwordx4 v[2:3], off
	v_and_b32_e32 v2, 64, v0
	v_mov_b32_e32 v3, 0x60
	v_cmp_ne_u32_e32 vcc, 0, v2
	v_bfe_u32 v153, v0, 5, 1
	v_lshrrev_b32_e32 v157, 1, v0
	v_cndmask_b32_e32 v151, 0, v3, vcc
	v_lshlrev_b32_e32 v3, 6, v0
	v_or_b32_e32 v2, v151, v156
	v_and_b32_e32 v115, 0x6000, v3
	v_bfe_u32 v3, v0, 4, 1
	v_lshlrev_b32_e32 v152, 7, v2
	v_or_b32_e32 v2, 6, v153
	v_bitop3_b32 v3, v157, v3, 7 bitop3:0x6c
	s_load_dwordx2 s[6:7], s[0:1], 0x28
	v_xor_b32_e32 v2, v2, v3
	v_lshlrev_b32_e32 v154, 4, v2
	v_or_b32_e32 v2, 4, v153
	v_xor_b32_e32 v2, v2, v3
	v_lshlrev_b32_e32 v155, 4, v2
	v_or_b32_e32 v2, 2, v153
	s_cmp_lt_u32 s2, 64
	v_xor_b32_e32 v2, v2, v3
	s_cselect_b64 s[4:5], -1, 0
	s_cmp_eq_u32 s36, 1
	v_lshlrev_b32_e32 v18, 4, v2
	v_xor_b32_e32 v2, v3, v153
	s_waitcnt lgkmcnt(0)
	s_cselect_b32 s18, s18, s6
	s_cselect_b32 s19, s19, s7
	s_and_b64 s[6:7], s[4:5], exec
	v_and_b32_e32 v1, 63, v0
	v_lshlrev_b32_e32 v150, 7, v156
	v_lshlrev_b32_e32 v2, 4, v2
	s_cselect_b32 s7, s17, s19
	s_cselect_b32 s6, s16, s18
	v_or_b32_e32 v182, v2, v152
	v_or_b32_e32 v2, v2, v115
	v_add_u32_e32 v112, v2, v150
	ds_read_b128 v[2:5], v112
	v_or_b32_e32 v116, 0x10000, v182
	v_add_u32_e32 v117, 0x11000, v182
	v_add_u32_e32 v118, 0x12000, v182
	ds_read_b128 v[6:9], v116
	ds_read_b128 v[10:13], v117
	ds_read_b128 v[14:17], v112 offset:4096
	ds_read_b128 v[122:125], v118
	v_or_b32_e32 v19, v18, v115
	v_add_u32_e32 v113, v19, v150
	s_waitcnt lgkmcnt(0)
	v_mfma_f32_32x32x16_f16 v[82:97], v[2:5], v[6:9], 0
	ds_read_b128 v[126:129], v113
	v_or_b32_e32 v183, v18, v152
	v_add_u32_e32 v120, 0x11000, v183
	v_or_b32_e32 v119, 0x10000, v183
	ds_read_b128 v[130:133], v113 offset:4096
	ds_read_b128 v[158:161], v119
	v_add_u32_e32 v121, 0x12000, v183
	ds_read_b128 v[162:165], v120
	ds_read_b128 v[166:169], v121
	v_mfma_f32_32x32x16_f16 v[66:81], v[2:5], v[10:13], 0
	v_mfma_f32_32x32x16_f16 v[50:65], v[2:5], v[122:125], 0
	v_mfma_f32_32x32x16_f16 v[34:49], v[14:17], v[6:9], 0
	v_mfma_f32_32x32x16_f16 v[18:33], v[14:17], v[10:13], 0
	v_mfma_f32_32x32x16_f16 v[2:17], v[14:17], v[122:125], 0
	s_waitcnt lgkmcnt(0)
	v_mfma_f32_32x32x16_f16 v[82:97], v[126:129], v[158:161], v[82:97]
	v_or_b32_e32 v114, v155, v115
	v_or_b32_e32 v155, v155, v152
	v_add_u32_e32 v114, v114, v150
	v_or_b32_e32 v122, 0x10000, v155
	v_add_u32_e32 v123, 0x11000, v155
	v_add_u32_e32 v124, 0x12000, v155
	v_mfma_f32_32x32x16_f16 v[66:81], v[126:129], v[162:165], v[66:81]
	v_mfma_f32_32x32x16_f16 v[50:65], v[126:129], v[166:169], v[50:65]
	v_mfma_f32_32x32x16_f16 v[34:49], v[130:133], v[158:161], v[34:49]
	ds_read_b128 v[126:129], v114
	ds_read_b128 v[158:161], v114 offset:4096
	v_mfma_f32_32x32x16_f16 v[18:33], v[130:133], v[162:165], v[18:33]
	ds_read_b128 v[162:165], v122
	ds_read_b128 v[170:173], v123
	ds_read_b128 v[174:177], v124
	v_mfma_f32_32x32x16_f16 v[2:17], v[130:133], v[166:169], v[2:17]
	s_waitcnt lgkmcnt(0)
	v_mfma_f32_32x32x16_f16 v[82:97], v[126:129], v[162:165], v[82:97]
	v_or_b32_e32 v115, v154, v115
	v_or_b32_e32 v133, v154, v152
	v_add_u32_e32 v115, v115, v150
	v_or_b32_e32 v125, 0x10000, v133
	v_mfma_f32_32x32x16_f16 v[66:81], v[126:129], v[170:173], v[66:81]
	v_mfma_f32_32x32x16_f16 v[50:65], v[126:129], v[174:177], v[50:65]
	v_add_u32_e32 v126, 0x11000, v133
	v_add_u32_e32 v127, 0x12000, v133
	v_mfma_f32_32x32x16_f16 v[34:49], v[158:161], v[162:165], v[34:49]
	ds_read_b128 v[128:131], v115
	ds_read_b128 v[162:165], v115 offset:4096
	v_mfma_f32_32x32x16_f16 v[18:33], v[158:161], v[170:173], v[18:33]
	ds_read_b128 v[166:169], v125
	ds_read_b128 v[170:173], v126
	ds_read_b128 v[178:181], v127
	v_mfma_f32_32x32x16_f16 v[2:17], v[158:161], v[174:177], v[2:17]
	s_waitcnt lgkmcnt(0)
	v_mfma_f32_32x32x16_f16 v[82:97], v[128:131], v[166:169], v[82:97]
	v_mfma_f32_32x32x16_f16 v[66:81], v[128:131], v[170:173], v[66:81]
	v_mfma_f32_32x32x16_f16 v[50:65], v[128:131], v[178:181], v[50:65]
	v_mfma_f32_32x32x16_f16 v[34:49], v[162:165], v[166:169], v[34:49]
	v_mfma_f32_32x32x16_f16 v[18:33], v[162:165], v[170:173], v[18:33]
	v_mfma_f32_32x32x16_f16 v[2:17], v[162:165], v[178:181], v[2:17]
	s_mov_b64 s[16:17], 0x100
	s_mov_b32 m0, s33
	v_lshl_add_u64 v[128:129], v[98:99], 0, s[16:17]
	s_waitcnt vmcnt(0)
	s_waitcnt vmcnt(0)
	s_barrier
	global_load_lds_dwordx4 v[128:129], off
	v_lshl_add_u64 v[128:129], v[100:101], 0, s[16:17]
	s_mov_b32 m0, s28
	s_nop 0
	global_load_lds_dwordx4 v[128:129], off
	v_lshl_add_u64 v[128:129], v[102:103], 0, s[16:17]
	s_mov_b32 m0, s29
	s_nop 0
	global_load_lds_dwordx4 v[128:129], off
	v_lshl_add_u64 v[128:129], v[104:105], 0, s[16:17]
	s_mov_b32 m0, s30
	s_nop 0
	global_load_lds_dwordx4 v[128:129], off
	v_lshl_add_u64 v[128:129], v[106:107], 0, s[16:17]
	s_mov_b32 m0, s31
	s_nop 0
	global_load_lds_dwordx4 v[128:129], off
	v_lshl_add_u64 v[128:129], v[108:109], 0, s[16:17]
	s_mov_b32 m0, s34
	s_nop 0
	global_load_lds_dwordx4 v[128:129], off
	v_lshl_add_u64 v[128:129], v[110:111], 0, s[16:17]
	s_mov_b32 m0, s35
	s_nop 0
	global_load_lds_dwordx4 v[128:129], off
	ds_read_b128 v[158:161], v112 offset:32768
	v_add_u32_e32 v129, 0x16000, v182
	v_add_u32_e32 v130, 0x17000, v182
	v_or_b32_e32 v131, 0x18000, v182
	ds_read_b128 v[162:165], v129
	ds_read_b128 v[166:169], v112 offset:36864
	ds_read_b128 v[170:173], v130
	ds_read_b128 v[174:177], v131
	v_add_u32_e32 v128, 0x16000, v183
	ds_read_b128 v[178:181], v128
	s_waitcnt lgkmcnt(0)
	v_mfma_f32_32x32x16_f16 v[82:97], v[158:161], v[162:165], v[82:97]
	v_mfma_f32_32x32x16_f16 v[66:81], v[158:161], v[170:173], v[66:81]
	v_mfma_f32_32x32x16_f16 v[50:65], v[158:161], v[174:177], v[50:65]
	v_mfma_f32_32x32x16_f16 v[34:49], v[166:169], v[162:165], v[34:49]
	v_mfma_f32_32x32x16_f16 v[18:33], v[166:169], v[170:173], v[18:33]
	ds_read_b128 v[158:161], v113 offset:32768
	ds_read_b128 v[162:165], v113 offset:36864
	ds_read_b128 v[170:173], v128 offset:4096
	ds_read_b128 v[182:185], v128 offset:8192
	v_mfma_f32_32x32x16_f16 v[2:17], v[166:169], v[174:177], v[2:17]
	s_waitcnt lgkmcnt(0)
	v_mfma_f32_32x32x16_f16 v[82:97], v[158:161], v[178:181], v[82:97]
	v_add_u32_e32 v132, 0x16000, v155
	v_mfma_f32_32x32x16_f16 v[66:81], v[158:161], v[170:173], v[66:81]
	v_mfma_f32_32x32x16_f16 v[50:65], v[158:161], v[182:185], v[50:65]
	ds_read_b128 v[158:161], v114 offset:32768
	ds_read_b128 v[166:169], v114 offset:36864
	v_mfma_f32_32x32x16_f16 v[34:49], v[162:165], v[178:181], v[34:49]
	v_mfma_f32_32x32x16_f16 v[18:33], v[162:165], v[170:173], v[18:33]
	ds_read_b128 v[170:173], v132
	ds_read_b128 v[174:177], v132 offset:4096
	ds_read_b128 v[178:181], v132 offset:8192
	v_mfma_f32_32x32x16_f16 v[2:17], v[162:165], v[182:185], v[2:17]
	s_waitcnt lgkmcnt(0)
	v_mfma_f32_32x32x16_f16 v[82:97], v[158:161], v[170:173], v[82:97]
	v_add_u32_e32 v133, 0x16000, v133
	v_mfma_f32_32x32x16_f16 v[66:81], v[158:161], v[174:177], v[66:81]
	v_mfma_f32_32x32x16_f16 v[50:65], v[158:161], v[178:181], v[50:65]
	ds_read_b128 v[158:161], v115 offset:32768
	ds_read_b128 v[162:165], v115 offset:36864
	v_mfma_f32_32x32x16_f16 v[34:49], v[166:169], v[170:173], v[34:49]
	v_mfma_f32_32x32x16_f16 v[18:33], v[166:169], v[174:177], v[18:33]
	ds_read_b128 v[170:173], v133
	ds_read_b128 v[174:177], v133 offset:4096
	ds_read_b128 v[182:185], v133 offset:8192
	v_mfma_f32_32x32x16_f16 v[2:17], v[166:169], v[178:181], v[2:17]
	s_waitcnt lgkmcnt(0)
	v_mfma_f32_32x32x16_f16 v[82:97], v[158:161], v[170:173], v[82:97]
	v_mfma_f32_32x32x16_f16 v[66:81], v[158:161], v[174:177], v[66:81]
	v_mfma_f32_32x32x16_f16 v[50:65], v[158:161], v[182:185], v[50:65]
	v_mfma_f32_32x32x16_f16 v[34:49], v[162:165], v[170:173], v[34:49]
	v_mfma_f32_32x32x16_f16 v[18:33], v[162:165], v[174:177], v[18:33]
	v_mfma_f32_32x32x16_f16 v[2:17], v[162:165], v[182:185], v[2:17]
	s_mov_b64 s[16:17], 0x180
	s_mov_b32 m0, s24
	v_lshl_add_u64 v[154:155], v[98:99], 0, s[16:17]
	s_waitcnt vmcnt(0)
	s_waitcnt vmcnt(0)
	s_barrier
	global_load_lds_dwordx4 v[154:155], off
	v_lshl_add_u64 v[154:155], v[100:101], 0, s[16:17]
	s_mov_b32 m0, s21
	s_nop 0
	global_load_lds_dwordx4 v[154:155], off
	v_lshl_add_u64 v[154:155], v[102:103], 0, s[16:17]
	s_mov_b32 m0, s22
	s_nop 0
	global_load_lds_dwordx4 v[154:155], off
	v_lshl_add_u64 v[154:155], v[104:105], 0, s[16:17]
	s_mov_b32 m0, s23
	s_nop 0
	global_load_lds_dwordx4 v[154:155], off
	v_lshl_add_u64 v[154:155], v[106:107], 0, s[16:17]
	s_mov_b32 m0, s25
	s_nop 0
	global_load_lds_dwordx4 v[154:155], off
	v_lshl_add_u64 v[154:155], v[108:109], 0, s[16:17]
	s_mov_b32 m0, s26
	s_nop 0
	global_load_lds_dwordx4 v[154:155], off
	v_lshl_add_u64 v[154:155], v[110:111], 0, s[16:17]
	s_mov_b32 m0, s27
	s_nop 0
	global_load_lds_dwordx4 v[154:155], off
	ds_read_b128 v[158:161], v112
	ds_read_b128 v[162:165], v116
	ds_read_b128 v[166:169], v112 offset:4096
	ds_read_b128 v[170:173], v117
	ds_read_b128 v[174:177], v118
	ds_read_b128 v[178:181], v113
	s_waitcnt lgkmcnt(0)
	v_mfma_f32_32x32x16_f16 v[82:97], v[158:161], v[162:165], v[82:97]
	v_mfma_f32_32x32x16_f16 v[66:81], v[158:161], v[170:173], v[66:81]
	v_mfma_f32_32x32x16_f16 v[50:65], v[158:161], v[174:177], v[50:65]
	v_mfma_f32_32x32x16_f16 v[34:49], v[166:169], v[162:165], v[34:49]
	v_mfma_f32_32x32x16_f16 v[18:33], v[166:169], v[170:173], v[18:33]
	ds_read_b128 v[158:161], v113 offset:4096
	ds_read_b128 v[162:165], v119
	ds_read_b128 v[170:173], v120
	ds_read_b128 v[182:185], v121
	v_mfma_f32_32x32x16_f16 v[2:17], v[166:169], v[174:177], v[2:17]
	s_waitcnt lgkmcnt(0)
	v_mfma_f32_32x32x16_f16 v[82:97], v[178:181], v[162:165], v[82:97]
	v_mfma_f32_32x32x16_f16 v[66:81], v[178:181], v[170:173], v[66:81]
	v_mfma_f32_32x32x16_f16 v[50:65], v[178:181], v[182:185], v[50:65]
	v_mfma_f32_32x32x16_f16 v[34:49], v[158:161], v[162:165], v[34:49]
	v_mfma_f32_32x32x16_f16 v[18:33], v[158:161], v[170:173], v[18:33]
	ds_read_b128 v[162:165], v114
	ds_read_b128 v[166:169], v114 offset:4096
	ds_read_b128 v[170:173], v122
	ds_read_b128 v[174:177], v123
	ds_read_b128 v[178:181], v124
	v_mfma_f32_32x32x16_f16 v[2:17], v[158:161], v[182:185], v[2:17]
	s_waitcnt lgkmcnt(0)
	v_mfma_f32_32x32x16_f16 v[82:97], v[162:165], v[170:173], v[82:97]
	v_mfma_f32_32x32x16_f16 v[66:81], v[162:165], v[174:177], v[66:81]
	v_mfma_f32_32x32x16_f16 v[50:65], v[162:165], v[178:181], v[50:65]
	v_mfma_f32_32x32x16_f16 v[34:49], v[166:169], v[170:173], v[34:49]
	v_mfma_f32_32x32x16_f16 v[18:33], v[166:169], v[174:177], v[18:33]
	ds_read_b128 v[158:161], v115
	ds_read_b128 v[162:165], v115 offset:4096
	ds_read_b128 v[170:173], v125
	ds_read_b128 v[174:177], v126
	ds_read_b128 v[182:185], v127
	v_mfma_f32_32x32x16_f16 v[2:17], v[166:169], v[178:181], v[2:17]
	s_waitcnt lgkmcnt(0)
	v_mfma_f32_32x32x16_f16 v[82:97], v[158:161], v[170:173], v[82:97]
	v_mfma_f32_32x32x16_f16 v[66:81], v[158:161], v[174:177], v[66:81]
	v_mfma_f32_32x32x16_f16 v[50:65], v[158:161], v[182:185], v[50:65]
	v_mfma_f32_32x32x16_f16 v[34:49], v[162:165], v[170:173], v[34:49]
	v_mfma_f32_32x32x16_f16 v[18:33], v[162:165], v[174:177], v[18:33]
	v_mfma_f32_32x32x16_f16 v[2:17], v[162:165], v[182:185], v[2:17]
	s_mov_b64 s[16:17], 0x200
	s_mov_b32 m0, s33
	v_lshl_add_u64 v[154:155], v[98:99], 0, s[16:17]
	s_waitcnt vmcnt(0)
	s_waitcnt vmcnt(0)
	s_barrier
	global_load_lds_dwordx4 v[154:155], off
	v_lshl_add_u64 v[154:155], v[100:101], 0, s[16:17]
	s_mov_b32 m0, s28
	s_nop 0
	global_load_lds_dwordx4 v[154:155], off
	v_lshl_add_u64 v[154:155], v[102:103], 0, s[16:17]
	s_mov_b32 m0, s29
	s_nop 0
	global_load_lds_dwordx4 v[154:155], off
	v_lshl_add_u64 v[154:155], v[104:105], 0, s[16:17]
	s_mov_b32 m0, s30
	s_nop 0
	global_load_lds_dwordx4 v[154:155], off
	v_lshl_add_u64 v[154:155], v[106:107], 0, s[16:17]
	s_mov_b32 m0, s31
	s_nop 0
	global_load_lds_dwordx4 v[154:155], off
	v_lshl_add_u64 v[154:155], v[108:109], 0, s[16:17]
	s_mov_b32 m0, s34
	s_nop 0
	global_load_lds_dwordx4 v[154:155], off
	v_lshl_add_u64 v[154:155], v[110:111], 0, s[16:17]
	s_mov_b32 m0, s35
	s_nop 0
	global_load_lds_dwordx4 v[154:155], off
	ds_read_b128 v[158:161], v112 offset:32768
	ds_read_b128 v[162:165], v129
	ds_read_b128 v[166:169], v112 offset:36864
	ds_read_b128 v[170:173], v130
	ds_read_b128 v[174:177], v131
	ds_read_b128 v[178:181], v128
	s_waitcnt lgkmcnt(0)
	v_mfma_f32_32x32x16_f16 v[82:97], v[158:161], v[162:165], v[82:97]
	v_mfma_f32_32x32x16_f16 v[66:81], v[158:161], v[170:173], v[66:81]
	v_mfma_f32_32x32x16_f16 v[50:65], v[158:161], v[174:177], v[50:65]
	v_mfma_f32_32x32x16_f16 v[34:49], v[166:169], v[162:165], v[34:49]
	v_mfma_f32_32x32x16_f16 v[18:33], v[166:169], v[170:173], v[18:33]
	ds_read_b128 v[158:161], v113 offset:32768
	ds_read_b128 v[162:165], v113 offset:36864
	ds_read_b128 v[170:173], v128 offset:4096
	ds_read_b128 v[182:185], v128 offset:8192
	v_mfma_f32_32x32x16_f16 v[2:17], v[166:169], v[174:177], v[2:17]
	s_waitcnt lgkmcnt(0)
	v_mfma_f32_32x32x16_f16 v[82:97], v[158:161], v[178:181], v[82:97]
	v_mfma_f32_32x32x16_f16 v[66:81], v[158:161], v[170:173], v[66:81]
	v_mfma_f32_32x32x16_f16 v[50:65], v[158:161], v[182:185], v[50:65]
	v_mfma_f32_32x32x16_f16 v[34:49], v[162:165], v[178:181], v[34:49]
	v_mfma_f32_32x32x16_f16 v[18:33], v[162:165], v[170:173], v[18:33]
	ds_read_b128 v[158:161], v114 offset:32768
	ds_read_b128 v[166:169], v114 offset:36864
	ds_read_b128 v[170:173], v132
	ds_read_b128 v[174:177], v132 offset:4096
	ds_read_b128 v[178:181], v132 offset:8192
	v_mfma_f32_32x32x16_f16 v[2:17], v[162:165], v[182:185], v[2:17]
	s_waitcnt lgkmcnt(0)
	v_mfma_f32_32x32x16_f16 v[82:97], v[158:161], v[170:173], v[82:97]
	v_mfma_f32_32x32x16_f16 v[66:81], v[158:161], v[174:177], v[66:81]
	v_mfma_f32_32x32x16_f16 v[50:65], v[158:161], v[178:181], v[50:65]
	v_mfma_f32_32x32x16_f16 v[34:49], v[166:169], v[170:173], v[34:49]
	v_mfma_f32_32x32x16_f16 v[18:33], v[166:169], v[174:177], v[18:33]
	ds_read_b128 v[158:161], v115 offset:32768
	ds_read_b128 v[162:165], v115 offset:36864
	ds_read_b128 v[170:173], v133
	ds_read_b128 v[174:177], v133 offset:4096
	ds_read_b128 v[182:185], v133 offset:8192
	v_mfma_f32_32x32x16_f16 v[2:17], v[166:169], v[178:181], v[2:17]
	s_waitcnt lgkmcnt(0)
	v_mfma_f32_32x32x16_f16 v[82:97], v[158:161], v[170:173], v[82:97]
	v_mfma_f32_32x32x16_f16 v[66:81], v[158:161], v[174:177], v[66:81]
	v_mfma_f32_32x32x16_f16 v[50:65], v[158:161], v[182:185], v[50:65]
	v_mfma_f32_32x32x16_f16 v[34:49], v[162:165], v[170:173], v[34:49]
	v_mfma_f32_32x32x16_f16 v[18:33], v[162:165], v[174:177], v[18:33]
	v_mfma_f32_32x32x16_f16 v[2:17], v[162:165], v[182:185], v[2:17]
	s_mov_b64 s[16:17], 0x280
	s_mov_b32 m0, s24
	v_lshl_add_u64 v[154:155], v[98:99], 0, s[16:17]
	s_waitcnt vmcnt(0)
	s_waitcnt vmcnt(0)
	s_barrier
	global_load_lds_dwordx4 v[154:155], off
	v_lshl_add_u64 v[154:155], v[100:101], 0, s[16:17]
	s_mov_b32 m0, s21
	s_nop 0
	global_load_lds_dwordx4 v[154:155], off
	v_lshl_add_u64 v[154:155], v[102:103], 0, s[16:17]
	s_mov_b32 m0, s22
	s_nop 0
	global_load_lds_dwordx4 v[154:155], off
	v_lshl_add_u64 v[154:155], v[104:105], 0, s[16:17]
	s_mov_b32 m0, s23
	s_nop 0
	global_load_lds_dwordx4 v[154:155], off
	v_lshl_add_u64 v[154:155], v[106:107], 0, s[16:17]
	s_mov_b32 m0, s25
	s_nop 0
	global_load_lds_dwordx4 v[154:155], off
	v_lshl_add_u64 v[154:155], v[108:109], 0, s[16:17]
	s_mov_b32 m0, s26
	s_nop 0
	global_load_lds_dwordx4 v[154:155], off
	v_lshl_add_u64 v[154:155], v[110:111], 0, s[16:17]
	s_mov_b32 m0, s27
	s_nop 0
	global_load_lds_dwordx4 v[154:155], off
	ds_read_b128 v[158:161], v112
	ds_read_b128 v[162:165], v116
	ds_read_b128 v[166:169], v112 offset:4096
	ds_read_b128 v[170:173], v117
	ds_read_b128 v[174:177], v118
	ds_read_b128 v[178:181], v113
	s_waitcnt lgkmcnt(0)
	v_mfma_f32_32x32x16_f16 v[82:97], v[158:161], v[162:165], v[82:97]
	v_mfma_f32_32x32x16_f16 v[66:81], v[158:161], v[170:173], v[66:81]
	v_mfma_f32_32x32x16_f16 v[50:65], v[158:161], v[174:177], v[50:65]
	v_mfma_f32_32x32x16_f16 v[34:49], v[166:169], v[162:165], v[34:49]
	v_mfma_f32_32x32x16_f16 v[18:33], v[166:169], v[170:173], v[18:33]
	ds_read_b128 v[158:161], v113 offset:4096
	ds_read_b128 v[162:165], v119
	ds_read_b128 v[170:173], v120
	ds_read_b128 v[182:185], v121
	v_mfma_f32_32x32x16_f16 v[2:17], v[166:169], v[174:177], v[2:17]
	s_waitcnt lgkmcnt(0)
	v_mfma_f32_32x32x16_f16 v[82:97], v[178:181], v[162:165], v[82:97]
	v_mfma_f32_32x32x16_f16 v[66:81], v[178:181], v[170:173], v[66:81]
	v_mfma_f32_32x32x16_f16 v[50:65], v[178:181], v[182:185], v[50:65]
	v_mfma_f32_32x32x16_f16 v[34:49], v[158:161], v[162:165], v[34:49]
	v_mfma_f32_32x32x16_f16 v[18:33], v[158:161], v[170:173], v[18:33]
	ds_read_b128 v[162:165], v114
	ds_read_b128 v[166:169], v114 offset:4096
	ds_read_b128 v[170:173], v122
	ds_read_b128 v[174:177], v123
	ds_read_b128 v[178:181], v124
	v_mfma_f32_32x32x16_f16 v[2:17], v[158:161], v[182:185], v[2:17]
	s_waitcnt lgkmcnt(0)
	v_mfma_f32_32x32x16_f16 v[82:97], v[162:165], v[170:173], v[82:97]
	v_mfma_f32_32x32x16_f16 v[66:81], v[162:165], v[174:177], v[66:81]
	v_mfma_f32_32x32x16_f16 v[50:65], v[162:165], v[178:181], v[50:65]
	v_mfma_f32_32x32x16_f16 v[34:49], v[166:169], v[170:173], v[34:49]
	v_mfma_f32_32x32x16_f16 v[18:33], v[166:169], v[174:177], v[18:33]
	ds_read_b128 v[158:161], v115
	ds_read_b128 v[162:165], v115 offset:4096
	ds_read_b128 v[170:173], v125
	ds_read_b128 v[174:177], v126
	ds_read_b128 v[182:185], v127
	v_mfma_f32_32x32x16_f16 v[2:17], v[166:169], v[178:181], v[2:17]
	s_waitcnt lgkmcnt(0)
	v_mfma_f32_32x32x16_f16 v[82:97], v[158:161], v[170:173], v[82:97]
	v_mfma_f32_32x32x16_f16 v[66:81], v[158:161], v[174:177], v[66:81]
	v_mfma_f32_32x32x16_f16 v[50:65], v[158:161], v[182:185], v[50:65]
	v_mfma_f32_32x32x16_f16 v[34:49], v[162:165], v[170:173], v[34:49]
	v_mfma_f32_32x32x16_f16 v[18:33], v[162:165], v[174:177], v[18:33]
	v_mfma_f32_32x32x16_f16 v[2:17], v[162:165], v[182:185], v[2:17]
	s_mov_b64 s[22:23], 0x300
	v_readfirstlane_b32 s24, v141
	v_lshl_add_u64 v[154:155], v[98:99], 0, s[22:23]
	s_mov_b32 m0, s24
	v_readfirstlane_b32 s16, v142
	s_waitcnt vmcnt(0)
	s_waitcnt vmcnt(0)
	s_barrier
	global_load_lds_dwordx4 v[154:155], off
	v_lshl_add_u64 v[154:155], v[100:101], 0, s[22:23]
	s_mov_b32 m0, s16
	v_readfirstlane_b32 s17, v143
	global_load_lds_dwordx4 v[154:155], off
	v_lshl_add_u64 v[154:155], v[102:103], 0, s[22:23]
	s_mov_b32 m0, s17
	v_readfirstlane_b32 s18, v144
	global_load_lds_dwordx4 v[154:155], off
	v_lshl_add_u64 v[142:143], v[104:105], 0, s[22:23]
	s_mov_b32 m0, s18
	v_readfirstlane_b32 s19, v145
	global_load_lds_dwordx4 v[142:143], off
	v_lshl_add_u64 v[142:143], v[106:107], 0, s[22:23]
	s_mov_b32 m0, s19
	v_readfirstlane_b32 s21, v146
	global_load_lds_dwordx4 v[142:143], off
	v_lshl_add_u64 v[142:143], v[108:109], 0, s[22:23]
	s_mov_b32 m0, s21
	s_nop 0
	global_load_lds_dwordx4 v[142:143], off
	v_lshl_add_u64 v[142:143], v[110:111], 0, s[22:23]
	v_readfirstlane_b32 s22, v148
	s_mov_b32 m0, s22
	s_nop 0
	global_load_lds_dwordx4 v[142:143], off
	ds_read_b128 v[142:145], v112 offset:32768
	ds_read_b128 v[158:161], v129
	ds_read_b128 v[162:165], v112 offset:36864
	ds_read_b128 v[166:169], v130
	ds_read_b128 v[170:173], v131
	ds_read_b128 v[174:177], v128
	s_waitcnt lgkmcnt(0)
	v_mfma_f32_32x32x16_f16 v[82:97], v[142:145], v[158:161], v[82:97]
	v_mfma_f32_32x32x16_f16 v[66:81], v[142:145], v[166:169], v[66:81]
	v_mfma_f32_32x32x16_f16 v[50:65], v[142:145], v[170:173], v[50:65]
	v_mfma_f32_32x32x16_f16 v[34:49], v[162:165], v[158:161], v[34:49]
	v_mfma_f32_32x32x16_f16 v[18:33], v[162:165], v[166:169], v[18:33]
	ds_read_b128 v[142:145], v113 offset:32768
	ds_read_b128 v[158:161], v113 offset:36864
	ds_read_b128 v[166:169], v128 offset:4096
	ds_read_b128 v[178:181], v128 offset:8192
	v_mfma_f32_32x32x16_f16 v[2:17], v[162:165], v[170:173], v[2:17]
	s_waitcnt lgkmcnt(0)
	v_mfma_f32_32x32x16_f16 v[82:97], v[142:145], v[174:177], v[82:97]
	v_mfma_f32_32x32x16_f16 v[66:81], v[142:145], v[166:169], v[66:81]
	v_mfma_f32_32x32x16_f16 v[50:65], v[142:145], v[178:181], v[50:65]
	v_mfma_f32_32x32x16_f16 v[34:49], v[158:161], v[174:177], v[34:49]
	v_mfma_f32_32x32x16_f16 v[18:33], v[158:161], v[166:169], v[18:33]
	ds_read_b128 v[142:145], v114 offset:32768
	ds_read_b128 v[162:165], v114 offset:36864
	ds_read_b128 v[166:169], v132
	ds_read_b128 v[170:173], v132 offset:4096
	ds_read_b128 v[174:177], v132 offset:8192
	v_mfma_f32_32x32x16_f16 v[2:17], v[158:161], v[178:181], v[2:17]
	s_waitcnt lgkmcnt(0)
	v_mfma_f32_32x32x16_f16 v[82:97], v[142:145], v[166:169], v[82:97]
	v_mfma_f32_32x32x16_f16 v[66:81], v[142:145], v[170:173], v[66:81]
	v_mfma_f32_32x32x16_f16 v[50:65], v[142:145], v[174:177], v[50:65]
	v_mfma_f32_32x32x16_f16 v[34:49], v[162:165], v[166:169], v[34:49]
	v_mfma_f32_32x32x16_f16 v[18:33], v[162:165], v[170:173], v[18:33]
	ds_read_b128 v[142:145], v115 offset:32768
	ds_read_b128 v[158:161], v115 offset:36864
	ds_read_b128 v[166:169], v133
	ds_read_b128 v[170:173], v133 offset:4096
	ds_read_b128 v[178:181], v133 offset:8192
	v_mfma_f32_32x32x16_f16 v[2:17], v[162:165], v[174:177], v[2:17]
	s_waitcnt lgkmcnt(0)
	v_mfma_f32_32x32x16_f16 v[82:97], v[142:145], v[166:169], v[82:97]
	v_mfma_f32_32x32x16_f16 v[66:81], v[142:145], v[170:173], v[66:81]
	v_mfma_f32_32x32x16_f16 v[50:65], v[142:145], v[178:181], v[50:65]
	v_mfma_f32_32x32x16_f16 v[34:49], v[158:161], v[166:169], v[34:49]
	v_mfma_f32_32x32x16_f16 v[18:33], v[158:161], v[170:173], v[18:33]
	v_mfma_f32_32x32x16_f16 v[2:17], v[158:161], v[178:181], v[2:17]
	s_mov_b64 s[34:35], 0x380
	v_readfirstlane_b32 s30, v134
	v_lshl_add_u64 v[142:143], v[98:99], 0, s[34:35]
	s_mov_b32 m0, s30
	v_readfirstlane_b32 s23, v135
	s_waitcnt vmcnt(0)
	s_waitcnt vmcnt(0)
	s_barrier
	global_load_lds_dwordx4 v[142:143], off
	v_lshl_add_u64 v[142:143], v[100:101], 0, s[34:35]
	s_mov_b32 m0, s23
	v_readfirstlane_b32 s25, v136
	global_load_lds_dwordx4 v[142:143], off
	v_lshl_add_u64 v[134:135], v[102:103], 0, s[34:35]
	s_mov_b32 m0, s25
	v_readfirstlane_b32 s26, v137
	global_load_lds_dwordx4 v[134:135], off
	v_lshl_add_u64 v[134:135], v[104:105], 0, s[34:35]
	s_mov_b32 m0, s26
	v_readfirstlane_b32 s27, v138
	global_load_lds_dwordx4 v[134:135], off
	v_lshl_add_u64 v[134:135], v[106:107], 0, s[34:35]
	s_mov_b32 m0, s27
	v_readfirstlane_b32 s28, v139
	global_load_lds_dwordx4 v[134:135], off
	v_lshl_add_u64 v[134:135], v[108:109], 0, s[34:35]
	s_mov_b32 m0, s28
	v_readfirstlane_b32 s29, v140
	global_load_lds_dwordx4 v[134:135], off
	v_lshl_add_u64 v[134:135], v[110:111], 0, s[34:35]
	s_mov_b32 m0, s29
	s_nop 0
	global_load_lds_dwordx4 v[134:135], off
	ds_read_b128 v[134:137], v112
	ds_read_b128 v[138:141], v116
	ds_read_b128 v[142:145], v112 offset:4096
	ds_read_b128 v[158:161], v117
	ds_read_b128 v[162:165], v118
	ds_read_b128 v[166:169], v113
	s_waitcnt lgkmcnt(0)
	v_mfma_f32_32x32x16_f16 v[82:97], v[134:137], v[138:141], v[82:97]
	v_mfma_f32_32x32x16_f16 v[66:81], v[134:137], v[158:161], v[66:81]
	v_mfma_f32_32x32x16_f16 v[50:65], v[134:137], v[162:165], v[50:65]
	v_mfma_f32_32x32x16_f16 v[34:49], v[142:145], v[138:141], v[34:49]
	v_mfma_f32_32x32x16_f16 v[18:33], v[142:145], v[158:161], v[18:33]
	ds_read_b128 v[134:137], v113 offset:4096
	ds_read_b128 v[138:141], v119
	ds_read_b128 v[158:161], v120
	ds_read_b128 v[170:173], v121
	v_mfma_f32_32x32x16_f16 v[2:17], v[142:145], v[162:165], v[2:17]
	s_waitcnt lgkmcnt(0)
	v_mfma_f32_32x32x16_f16 v[82:97], v[166:169], v[138:141], v[82:97]
	v_mfma_f32_32x32x16_f16 v[66:81], v[166:169], v[158:161], v[66:81]
	v_mfma_f32_32x32x16_f16 v[50:65], v[166:169], v[170:173], v[50:65]
	v_mfma_f32_32x32x16_f16 v[34:49], v[134:137], v[138:141], v[34:49]
	v_mfma_f32_32x32x16_f16 v[18:33], v[134:137], v[158:161], v[18:33]
	ds_read_b128 v[138:141], v114
	ds_read_b128 v[142:145], v114 offset:4096
	ds_read_b128 v[158:161], v122
	ds_read_b128 v[162:165], v123
	ds_read_b128 v[166:169], v124
	v_mfma_f32_32x32x16_f16 v[2:17], v[134:137], v[170:173], v[2:17]
	s_waitcnt lgkmcnt(0)
	v_mfma_f32_32x32x16_f16 v[82:97], v[138:141], v[158:161], v[82:97]
	v_mfma_f32_32x32x16_f16 v[66:81], v[138:141], v[162:165], v[66:81]
	v_mfma_f32_32x32x16_f16 v[50:65], v[138:141], v[166:169], v[50:65]
	v_mfma_f32_32x32x16_f16 v[34:49], v[142:145], v[158:161], v[34:49]
	v_mfma_f32_32x32x16_f16 v[18:33], v[142:145], v[162:165], v[18:33]
	ds_read_b128 v[134:137], v115
	ds_read_b128 v[138:141], v115 offset:4096
	ds_read_b128 v[158:161], v125
	ds_read_b128 v[162:165], v126
	ds_read_b128 v[170:173], v127
	v_mfma_f32_32x32x16_f16 v[2:17], v[142:145], v[166:169], v[2:17]
	s_waitcnt lgkmcnt(0)
	v_mfma_f32_32x32x16_f16 v[82:97], v[134:137], v[158:161], v[82:97]
	v_mfma_f32_32x32x16_f16 v[66:81], v[134:137], v[162:165], v[66:81]
	v_mfma_f32_32x32x16_f16 v[50:65], v[134:137], v[170:173], v[50:65]
	v_mfma_f32_32x32x16_f16 v[34:49], v[138:141], v[158:161], v[34:49]
	v_mfma_f32_32x32x16_f16 v[18:33], v[138:141], v[162:165], v[18:33]
	v_mfma_f32_32x32x16_f16 v[2:17], v[138:141], v[170:173], v[2:17]
	s_mov_b64 s[34:35], 0x400
	s_mov_b32 m0, s24
	v_lshl_add_u64 v[134:135], v[98:99], 0, s[34:35]
	s_waitcnt vmcnt(0)
	s_waitcnt vmcnt(0)
	s_barrier
	global_load_lds_dwordx4 v[134:135], off
	v_lshl_add_u64 v[134:135], v[100:101], 0, s[34:35]
	s_mov_b32 m0, s16
	s_nop 0
	global_load_lds_dwordx4 v[134:135], off
	v_lshl_add_u64 v[134:135], v[102:103], 0, s[34:35]
	s_mov_b32 m0, s17
	s_nop 0
	global_load_lds_dwordx4 v[134:135], off
	v_lshl_add_u64 v[134:135], v[104:105], 0, s[34:35]
	s_mov_b32 m0, s18
	s_nop 0
	global_load_lds_dwordx4 v[134:135], off
	v_lshl_add_u64 v[134:135], v[106:107], 0, s[34:35]
	s_mov_b32 m0, s19
	s_nop 0
	global_load_lds_dwordx4 v[134:135], off
	v_lshl_add_u64 v[134:135], v[108:109], 0, s[34:35]
	s_mov_b32 m0, s21
	s_nop 0
	global_load_lds_dwordx4 v[134:135], off
	v_lshl_add_u64 v[134:135], v[110:111], 0, s[34:35]
	s_mov_b32 m0, s22
	s_nop 0
	global_load_lds_dwordx4 v[134:135], off
	ds_read_b128 v[134:137], v112 offset:32768
	ds_read_b128 v[138:141], v129
	ds_read_b128 v[142:145], v112 offset:36864
	ds_read_b128 v[158:161], v130
	ds_read_b128 v[162:165], v131
	ds_read_b128 v[166:169], v128
	s_waitcnt lgkmcnt(0)
	v_mfma_f32_32x32x16_f16 v[82:97], v[134:137], v[138:141], v[82:97]
	v_mfma_f32_32x32x16_f16 v[66:81], v[134:137], v[158:161], v[66:81]
	v_mfma_f32_32x32x16_f16 v[50:65], v[134:137], v[162:165], v[50:65]
	v_mfma_f32_32x32x16_f16 v[34:49], v[142:145], v[138:141], v[34:49]
	v_mfma_f32_32x32x16_f16 v[18:33], v[142:145], v[158:161], v[18:33]
	ds_read_b128 v[134:137], v113 offset:32768
	ds_read_b128 v[138:141], v113 offset:36864
	ds_read_b128 v[158:161], v128 offset:4096
	ds_read_b128 v[170:173], v128 offset:8192
	v_mfma_f32_32x32x16_f16 v[2:17], v[142:145], v[162:165], v[2:17]
	s_waitcnt lgkmcnt(0)
	v_mfma_f32_32x32x16_f16 v[82:97], v[134:137], v[166:169], v[82:97]
	v_mfma_f32_32x32x16_f16 v[66:81], v[134:137], v[158:161], v[66:81]
	v_mfma_f32_32x32x16_f16 v[50:65], v[134:137], v[170:173], v[50:65]
	v_mfma_f32_32x32x16_f16 v[34:49], v[138:141], v[166:169], v[34:49]
	v_mfma_f32_32x32x16_f16 v[18:33], v[138:141], v[158:161], v[18:33]
	ds_read_b128 v[134:137], v114 offset:32768
	ds_read_b128 v[142:145], v114 offset:36864
	ds_read_b128 v[158:161], v132
	ds_read_b128 v[162:165], v132 offset:4096
	ds_read_b128 v[166:169], v132 offset:8192
	v_mfma_f32_32x32x16_f16 v[2:17], v[138:141], v[170:173], v[2:17]
	s_waitcnt lgkmcnt(0)
	v_mfma_f32_32x32x16_f16 v[82:97], v[134:137], v[158:161], v[82:97]
	v_mfma_f32_32x32x16_f16 v[66:81], v[134:137], v[162:165], v[66:81]
	v_mfma_f32_32x32x16_f16 v[50:65], v[134:137], v[166:169], v[50:65]
	v_mfma_f32_32x32x16_f16 v[34:49], v[142:145], v[158:161], v[34:49]
	v_mfma_f32_32x32x16_f16 v[18:33], v[142:145], v[162:165], v[18:33]
	ds_read_b128 v[134:137], v115 offset:32768
	ds_read_b128 v[138:141], v115 offset:36864
	ds_read_b128 v[158:161], v133
	ds_read_b128 v[162:165], v133 offset:4096
	ds_read_b128 v[170:173], v133 offset:8192
	v_mfma_f32_32x32x16_f16 v[2:17], v[142:145], v[166:169], v[2:17]
	s_waitcnt lgkmcnt(0)
	v_mfma_f32_32x32x16_f16 v[82:97], v[134:137], v[158:161], v[82:97]
	v_mfma_f32_32x32x16_f16 v[66:81], v[134:137], v[162:165], v[66:81]
	v_mfma_f32_32x32x16_f16 v[50:65], v[134:137], v[170:173], v[50:65]
	v_mfma_f32_32x32x16_f16 v[34:49], v[138:141], v[158:161], v[34:49]
	v_mfma_f32_32x32x16_f16 v[18:33], v[138:141], v[162:165], v[18:33]
	v_mfma_f32_32x32x16_f16 v[2:17], v[138:141], v[170:173], v[2:17]
	s_mov_b64 s[34:35], 0x480
	s_mov_b32 m0, s30
	v_lshl_add_u64 v[134:135], v[98:99], 0, s[34:35]
	s_waitcnt vmcnt(0)
	s_waitcnt vmcnt(0)
	s_barrier
	global_load_lds_dwordx4 v[134:135], off
	v_lshl_add_u64 v[134:135], v[100:101], 0, s[34:35]
	s_mov_b32 m0, s23
	s_nop 0
	global_load_lds_dwordx4 v[134:135], off
	v_lshl_add_u64 v[134:135], v[102:103], 0, s[34:35]
	s_mov_b32 m0, s25
	s_nop 0
	global_load_lds_dwordx4 v[134:135], off
	v_lshl_add_u64 v[134:135], v[104:105], 0, s[34:35]
	s_mov_b32 m0, s26
	s_nop 0
	global_load_lds_dwordx4 v[134:135], off
	v_lshl_add_u64 v[134:135], v[106:107], 0, s[34:35]
	s_mov_b32 m0, s27
	s_nop 0
	global_load_lds_dwordx4 v[134:135], off
	v_lshl_add_u64 v[134:135], v[108:109], 0, s[34:35]
	s_mov_b32 m0, s28
	s_nop 0
	global_load_lds_dwordx4 v[134:135], off
	v_lshl_add_u64 v[134:135], v[110:111], 0, s[34:35]
	s_mov_b32 m0, s29
	s_nop 0
	global_load_lds_dwordx4 v[134:135], off
	ds_read_b128 v[134:137], v112
	ds_read_b128 v[138:141], v116
	ds_read_b128 v[142:145], v112 offset:4096
	ds_read_b128 v[158:161], v117
	ds_read_b128 v[162:165], v118
	ds_read_b128 v[166:169], v113
	s_waitcnt lgkmcnt(0)
	v_mfma_f32_32x32x16_f16 v[82:97], v[134:137], v[138:141], v[82:97]
	v_mfma_f32_32x32x16_f16 v[66:81], v[134:137], v[158:161], v[66:81]
	v_mfma_f32_32x32x16_f16 v[50:65], v[134:137], v[162:165], v[50:65]
	v_mfma_f32_32x32x16_f16 v[34:49], v[142:145], v[138:141], v[34:49]
	v_mfma_f32_32x32x16_f16 v[18:33], v[142:145], v[158:161], v[18:33]
	ds_read_b128 v[134:137], v113 offset:4096
	ds_read_b128 v[138:141], v119
	ds_read_b128 v[158:161], v120
	ds_read_b128 v[170:173], v121
	v_mfma_f32_32x32x16_f16 v[2:17], v[142:145], v[162:165], v[2:17]
	s_waitcnt lgkmcnt(0)
	v_mfma_f32_32x32x16_f16 v[82:97], v[166:169], v[138:141], v[82:97]
	v_mfma_f32_32x32x16_f16 v[66:81], v[166:169], v[158:161], v[66:81]
	v_mfma_f32_32x32x16_f16 v[50:65], v[166:169], v[170:173], v[50:65]
	v_mfma_f32_32x32x16_f16 v[34:49], v[134:137], v[138:141], v[34:49]
	v_mfma_f32_32x32x16_f16 v[18:33], v[134:137], v[158:161], v[18:33]
	ds_read_b128 v[138:141], v114
	ds_read_b128 v[142:145], v114 offset:4096
	ds_read_b128 v[158:161], v122
	ds_read_b128 v[162:165], v123
	ds_read_b128 v[166:169], v124
	v_mfma_f32_32x32x16_f16 v[2:17], v[134:137], v[170:173], v[2:17]
	s_waitcnt lgkmcnt(0)
	v_mfma_f32_32x32x16_f16 v[82:97], v[138:141], v[158:161], v[82:97]
	v_mfma_f32_32x32x16_f16 v[66:81], v[138:141], v[162:165], v[66:81]
	v_mfma_f32_32x32x16_f16 v[50:65], v[138:141], v[166:169], v[50:65]
	v_mfma_f32_32x32x16_f16 v[34:49], v[142:145], v[158:161], v[34:49]
	v_mfma_f32_32x32x16_f16 v[18:33], v[142:145], v[162:165], v[18:33]
	ds_read_b128 v[134:137], v115
	ds_read_b128 v[138:141], v115 offset:4096
	ds_read_b128 v[158:161], v125
	ds_read_b128 v[162:165], v126
	ds_read_b128 v[170:173], v127
	v_mfma_f32_32x32x16_f16 v[2:17], v[142:145], v[166:169], v[2:17]
	s_waitcnt lgkmcnt(0)
	v_mfma_f32_32x32x16_f16 v[82:97], v[134:137], v[158:161], v[82:97]
	v_mfma_f32_32x32x16_f16 v[66:81], v[134:137], v[162:165], v[66:81]
	v_mfma_f32_32x32x16_f16 v[50:65], v[134:137], v[170:173], v[50:65]
	v_mfma_f32_32x32x16_f16 v[34:49], v[138:141], v[158:161], v[34:49]
	v_mfma_f32_32x32x16_f16 v[18:33], v[138:141], v[162:165], v[18:33]
	v_mfma_f32_32x32x16_f16 v[2:17], v[138:141], v[170:173], v[2:17]
	s_mov_b64 s[34:35], 0x500
	s_mov_b32 m0, s24
	v_lshl_add_u64 v[134:135], v[98:99], 0, s[34:35]
	s_waitcnt vmcnt(0)
	s_waitcnt vmcnt(0)
	s_barrier
	global_load_lds_dwordx4 v[134:135], off
	v_lshl_add_u64 v[134:135], v[100:101], 0, s[34:35]
	s_mov_b32 m0, s16
	s_nop 0
	global_load_lds_dwordx4 v[134:135], off
	v_lshl_add_u64 v[134:135], v[102:103], 0, s[34:35]
	s_mov_b32 m0, s17
	s_nop 0
	global_load_lds_dwordx4 v[134:135], off
	v_lshl_add_u64 v[134:135], v[104:105], 0, s[34:35]
	s_mov_b32 m0, s18
	s_nop 0
	global_load_lds_dwordx4 v[134:135], off
	v_lshl_add_u64 v[134:135], v[106:107], 0, s[34:35]
	s_mov_b32 m0, s19
	s_nop 0
	global_load_lds_dwordx4 v[134:135], off
	v_lshl_add_u64 v[134:135], v[108:109], 0, s[34:35]
	s_mov_b32 m0, s21
	s_nop 0
	global_load_lds_dwordx4 v[134:135], off
	v_lshl_add_u64 v[134:135], v[110:111], 0, s[34:35]
	s_mov_b32 m0, s22
	s_nop 0
	global_load_lds_dwordx4 v[134:135], off
	ds_read_b128 v[134:137], v112 offset:32768
	ds_read_b128 v[138:141], v129
	ds_read_b128 v[142:145], v112 offset:36864
	ds_read_b128 v[158:161], v130
	ds_read_b128 v[162:165], v131
	ds_read_b128 v[166:169], v128
	s_waitcnt lgkmcnt(0)
	v_mfma_f32_32x32x16_f16 v[82:97], v[134:137], v[138:141], v[82:97]
	v_mfma_f32_32x32x16_f16 v[66:81], v[134:137], v[158:161], v[66:81]
	v_mfma_f32_32x32x16_f16 v[50:65], v[134:137], v[162:165], v[50:65]
	v_mfma_f32_32x32x16_f16 v[34:49], v[142:145], v[138:141], v[34:49]
	v_mfma_f32_32x32x16_f16 v[18:33], v[142:145], v[158:161], v[18:33]
	ds_read_b128 v[134:137], v113 offset:32768
	ds_read_b128 v[138:141], v113 offset:36864
	ds_read_b128 v[158:161], v128 offset:4096
	ds_read_b128 v[170:173], v128 offset:8192
	v_mfma_f32_32x32x16_f16 v[2:17], v[142:145], v[162:165], v[2:17]
	s_waitcnt lgkmcnt(0)
	v_mfma_f32_32x32x16_f16 v[82:97], v[134:137], v[166:169], v[82:97]
	v_mfma_f32_32x32x16_f16 v[66:81], v[134:137], v[158:161], v[66:81]
	v_mfma_f32_32x32x16_f16 v[50:65], v[134:137], v[170:173], v[50:65]
	v_mfma_f32_32x32x16_f16 v[34:49], v[138:141], v[166:169], v[34:49]
	v_mfma_f32_32x32x16_f16 v[18:33], v[138:141], v[158:161], v[18:33]
	ds_read_b128 v[134:137], v114 offset:32768
	ds_read_b128 v[142:145], v114 offset:36864
	ds_read_b128 v[158:161], v132
	ds_read_b128 v[162:165], v132 offset:4096
	ds_read_b128 v[166:169], v132 offset:8192
	v_mfma_f32_32x32x16_f16 v[2:17], v[138:141], v[170:173], v[2:17]
	s_waitcnt lgkmcnt(0)
	v_mfma_f32_32x32x16_f16 v[82:97], v[134:137], v[158:161], v[82:97]
	v_mfma_f32_32x32x16_f16 v[66:81], v[134:137], v[162:165], v[66:81]
	v_mfma_f32_32x32x16_f16 v[50:65], v[134:137], v[166:169], v[50:65]
	v_mfma_f32_32x32x16_f16 v[34:49], v[142:145], v[158:161], v[34:49]
	v_mfma_f32_32x32x16_f16 v[18:33], v[142:145], v[162:165], v[18:33]
	ds_read_b128 v[134:137], v115 offset:32768
	ds_read_b128 v[138:141], v115 offset:36864
	ds_read_b128 v[158:161], v133
	ds_read_b128 v[162:165], v133 offset:4096
	ds_read_b128 v[170:173], v133 offset:8192
	v_mfma_f32_32x32x16_f16 v[2:17], v[142:145], v[166:169], v[2:17]
	s_waitcnt lgkmcnt(0)
	v_mfma_f32_32x32x16_f16 v[82:97], v[134:137], v[158:161], v[82:97]
	v_mfma_f32_32x32x16_f16 v[66:81], v[134:137], v[162:165], v[66:81]
	v_mfma_f32_32x32x16_f16 v[50:65], v[134:137], v[170:173], v[50:65]
	v_mfma_f32_32x32x16_f16 v[34:49], v[138:141], v[158:161], v[34:49]
	v_mfma_f32_32x32x16_f16 v[18:33], v[138:141], v[162:165], v[18:33]
	v_mfma_f32_32x32x16_f16 v[2:17], v[138:141], v[170:173], v[2:17]
	s_mov_b64 s[16:17], 0x580
	s_mov_b32 m0, s30
	v_lshl_add_u64 v[98:99], v[98:99], 0, s[16:17]
	s_waitcnt vmcnt(0)
	s_waitcnt vmcnt(0)
	s_barrier
	global_load_lds_dwordx4 v[98:99], off
	v_lshl_add_u64 v[98:99], v[100:101], 0, s[16:17]
	s_mov_b32 m0, s23
	s_nop 0
	global_load_lds_dwordx4 v[98:99], off
	v_lshl_add_u64 v[98:99], v[102:103], 0, s[16:17]
	s_mov_b32 m0, s25
	s_nop 0
	global_load_lds_dwordx4 v[98:99], off
	v_lshl_add_u64 v[98:99], v[104:105], 0, s[16:17]
	s_mov_b32 m0, s26
	s_nop 0
	global_load_lds_dwordx4 v[98:99], off
	v_lshl_add_u64 v[98:99], v[106:107], 0, s[16:17]
	s_mov_b32 m0, s27
	s_nop 0
	global_load_lds_dwordx4 v[98:99], off
	v_lshl_add_u64 v[98:99], v[108:109], 0, s[16:17]
	s_mov_b32 m0, s28
	s_nop 0
	global_load_lds_dwordx4 v[98:99], off
	v_lshl_add_u64 v[98:99], v[110:111], 0, s[16:17]
	s_mov_b32 m0, s29
	s_nop 0
	global_load_lds_dwordx4 v[98:99], off
	ds_read_b128 v[98:101], v112
	ds_read_b128 v[102:105], v116
	ds_read_b128 v[106:109], v112 offset:4096
	ds_read_b128 v[134:137], v117
	ds_read_b128 v[138:141], v118
	ds_read_b128 v[142:145], v113
	s_waitcnt lgkmcnt(0)
	v_mfma_f32_32x32x16_f16 v[82:97], v[98:101], v[102:105], v[82:97]
	v_mfma_f32_32x32x16_f16 v[66:81], v[98:101], v[134:137], v[66:81]
	v_mfma_f32_32x32x16_f16 v[50:65], v[98:101], v[138:141], v[50:65]
	v_mfma_f32_32x32x16_f16 v[34:49], v[106:109], v[102:105], v[34:49]
	v_mfma_f32_32x32x16_f16 v[18:33], v[106:109], v[134:137], v[18:33]
	ds_read_b128 v[98:101], v113 offset:4096
	ds_read_b128 v[102:105], v119
	ds_read_b128 v[116:119], v120
	ds_read_b128 v[134:137], v121
	v_mfma_f32_32x32x16_f16 v[2:17], v[106:109], v[138:141], v[2:17]
	s_waitcnt lgkmcnt(0)
	v_mfma_f32_32x32x16_f16 v[82:97], v[142:145], v[102:105], v[82:97]
	v_mfma_f32_32x32x16_f16 v[66:81], v[142:145], v[116:119], v[66:81]
	v_mfma_f32_32x32x16_f16 v[50:65], v[142:145], v[134:137], v[50:65]
	v_mfma_f32_32x32x16_f16 v[34:49], v[98:101], v[102:105], v[34:49]
	v_mfma_f32_32x32x16_f16 v[18:33], v[98:101], v[116:119], v[18:33]
	ds_read_b128 v[102:105], v114
	ds_read_b128 v[106:109], v114 offset:4096
	ds_read_b128 v[116:119], v122
	ds_read_b128 v[120:123], v123
	ds_read_b128 v[138:141], v124
	v_mfma_f32_32x32x16_f16 v[2:17], v[98:101], v[134:137], v[2:17]
	s_waitcnt lgkmcnt(0)
	v_mfma_f32_32x32x16_f16 v[82:97], v[102:105], v[116:119], v[82:97]
	v_mfma_f32_32x32x16_f16 v[66:81], v[102:105], v[120:123], v[66:81]
	v_mfma_f32_32x32x16_f16 v[50:65], v[102:105], v[138:141], v[50:65]
	v_mfma_f32_32x32x16_f16 v[34:49], v[106:109], v[116:119], v[34:49]
	v_mfma_f32_32x32x16_f16 v[18:33], v[106:109], v[120:123], v[18:33]
	ds_read_b128 v[98:101], v115
	ds_read_b128 v[102:105], v115 offset:4096
	ds_read_b128 v[116:119], v125
	ds_read_b128 v[120:123], v126
	ds_read_b128 v[124:127], v127
	v_mfma_f32_32x32x16_f16 v[2:17], v[106:109], v[138:141], v[2:17]
	s_waitcnt lgkmcnt(0)
	v_mfma_f32_32x32x16_f16 v[82:97], v[98:101], v[116:119], v[82:97]
	v_mfma_f32_32x32x16_f16 v[66:81], v[98:101], v[120:123], v[66:81]
	v_mfma_f32_32x32x16_f16 v[50:65], v[98:101], v[124:127], v[50:65]
	v_mfma_f32_32x32x16_f16 v[34:49], v[102:105], v[116:119], v[34:49]
	v_mfma_f32_32x32x16_f16 v[18:33], v[102:105], v[120:123], v[18:33]
	v_mfma_f32_32x32x16_f16 v[2:17], v[102:105], v[124:127], v[2:17]
	s_waitcnt vmcnt(0)
	s_waitcnt vmcnt(0)
	s_barrier
	ds_read_b128 v[98:101], v112 offset:32768
	ds_read_b128 v[102:105], v129
	ds_read_b128 v[106:109], v112 offset:36864
	ds_read_b128 v[116:119], v130
	ds_read_b128 v[120:123], v131
	ds_read_b128 v[124:127], v128
	s_waitcnt lgkmcnt(4)
	v_mfma_f32_32x32x16_f16 v[82:97], v[98:101], v[102:105], v[82:97]
	s_waitcnt lgkmcnt(2)
	v_mfma_f32_32x32x16_f16 v[66:81], v[98:101], v[116:119], v[66:81]
	s_waitcnt lgkmcnt(1)
	v_mfma_f32_32x32x16_f16 v[50:65], v[98:101], v[120:123], v[50:65]
	v_mfma_f32_32x32x16_f16 v[34:49], v[106:109], v[102:105], v[34:49]
	v_mfma_f32_32x32x16_f16 v[18:33], v[106:109], v[116:119], v[18:33]
	ds_read_b128 v[98:101], v113 offset:32768
	ds_read_b128 v[102:105], v113 offset:36864
	ds_read_b128 v[110:113], v128 offset:4096
	ds_read_b128 v[116:119], v128 offset:8192
	v_mfma_f32_32x32x16_f16 v[2:17], v[106:109], v[120:123], v[2:17]
	s_waitcnt lgkmcnt(3)
	v_mfma_f32_32x32x16_f16 v[82:97], v[98:101], v[124:127], v[82:97]
	s_waitcnt lgkmcnt(1)
	v_mfma_f32_32x32x16_f16 v[66:81], v[98:101], v[110:113], v[66:81]
	s_waitcnt lgkmcnt(0)
	v_mfma_f32_32x32x16_f16 v[50:65], v[98:101], v[116:119], v[50:65]
	v_mfma_f32_32x32x16_f16 v[34:49], v[102:105], v[124:127], v[34:49]
	v_mfma_f32_32x32x16_f16 v[18:33], v[102:105], v[110:113], v[18:33]
	ds_read_b128 v[98:101], v114 offset:32768
	ds_read_b128 v[106:109], v114 offset:36864
	ds_read_b128 v[110:113], v132
	ds_read_b128 v[120:123], v132 offset:4096
	ds_read_b128 v[124:127], v132 offset:8192
	v_mfma_f32_32x32x16_f16 v[2:17], v[102:105], v[116:119], v[2:17]
	s_waitcnt lgkmcnt(2)
	v_mfma_f32_32x32x16_f16 v[82:97], v[98:101], v[110:113], v[82:97]
	s_waitcnt lgkmcnt(1)
	v_mfma_f32_32x32x16_f16 v[66:81], v[98:101], v[120:123], v[66:81]
	s_waitcnt lgkmcnt(0)
	v_mfma_f32_32x32x16_f16 v[50:65], v[98:101], v[124:127], v[50:65]
	v_mfma_f32_32x32x16_f16 v[34:49], v[106:109], v[110:113], v[34:49]
	v_mfma_f32_32x32x16_f16 v[18:33], v[106:109], v[120:123], v[18:33]
	ds_read_b128 v[98:101], v115 offset:32768
	ds_read_b128 v[102:105], v115 offset:36864
	ds_read_b128 v[110:113], v133
	ds_read_b128 v[114:117], v133 offset:4096
	ds_read_b128 v[118:121], v133 offset:8192
	v_mfma_f32_32x32x16_f16 v[2:17], v[106:109], v[124:127], v[2:17]
	s_waitcnt lgkmcnt(2)
	v_mfma_f32_32x32x16_f16 v[82:97], v[98:101], v[110:113], v[82:97]
	s_waitcnt lgkmcnt(1)
	v_mfma_f32_32x32x16_f16 v[66:81], v[98:101], v[114:117], v[66:81]
	s_waitcnt lgkmcnt(0)
	v_mfma_f32_32x32x16_f16 v[50:65], v[98:101], v[118:121], v[50:65]
	v_mfma_f32_32x32x16_f16 v[34:49], v[102:105], v[110:113], v[34:49]
	v_mfma_f32_32x32x16_f16 v[18:33], v[102:105], v[114:117], v[18:33]
	v_mfma_f32_32x32x16_f16 v[2:17], v[102:105], v[118:121], v[2:17]
	v_add_u32_e32 v158, s20, v151
	v_and_b32_e32 v154, 32, v0
	v_mov_b32_e32 v155, v147
	v_lshl_add_u64 v[98:99], s[6:7], 0, v[154:155]
	v_or_b32_e32 v100, v158, v156
	v_lshlrev_b32_e32 v146, 2, v158
	v_lshlrev_b32_e32 v100, 2, v100
	v_lshl_add_u64 v[102:103], v[98:99], 0, v[146:147]
	s_waitcnt vmcnt(0)
	s_barrier
	global_load_dwordx4 v[138:141], v[102:103], off offset:16
	global_load_dwordx4 v[134:137], v[102:103], off offset:64
	global_load_dwordx4 v[130:133], v[102:103], off offset:80
	global_load_dwordx4 v[126:129], v[102:103], off offset:128
	global_load_dwordx4 v[122:125], v[102:103], off offset:144
	global_load_dwordx4 v[118:121], v[102:103], off offset:192
	global_load_dword v152, v100, s[6:7]
	global_load_dwordx4 v[142:145], v[102:103], off
	global_load_dword v150, v100, s[6:7] offset:128
	global_load_dword v148, v100, s[6:7] offset:256
	global_load_dwordx4 v[114:117], v[102:103], off offset:208
	global_load_dwordx4 v[110:113], v[102:103], off offset:256
	s_nop 0
	global_load_dwordx4 v[98:101], v[102:103], off offset:336
	global_load_dwordx4 v[106:109], v[102:103], off offset:272
	s_nop 0
	global_load_dwordx4 v[102:105], v[102:103], off offset:320
	v_mul_u32_u24_e32 v146, 0x1200, v149
	v_mov_b32_e32 v155, 0x1c0
	s_movk_i32 s18, 0x1200
	v_lshl_or_b32 v146, v156, 2, v146
	s_bfe_u32 s6, s3, 0x30009
	v_bitop3_b32 v155, s3, v155, v157 bitop3:0xc8
	v_mul_u32_u24_e32 v156, 0x90, v156
	s_movk_i32 s3, 0x240
	v_mad_u32_u24 v156, v149, s18, v156
	v_mad_u32_u24 v149, v153, s3, v146
	v_mul_u32_u24_e64 v157, s6, 12
	s_cmpk_gt_u32 s2, 0x7f
	ds_write2_b32 v149, v82, v83 offset1:36
	ds_write2_b32 v149, v84, v85 offset0:72 offset1:108
	v_add_u32_e32 v153, 0x400, v149
	v_lshrrev_b32_e32 v83, 6, v158
	s_cselect_b64 s[16:17], -1, 0
	s_and_b64 s[6:7], s[4:5], exec
	ds_write2_b32 v153, v86, v87 offset0:32 offset1:68
	ds_write2_b32 v153, v88, v89 offset0:104 offset1:140
	v_add_u32_e32 v86, 0x800, v149
	v_and_b32_e32 v89, 32, v151
	v_add_lshl_u32 v146, v83, v157, 15
	s_cselect_b32 s7, s11, s13
	s_cselect_b32 s6, s10, s12
	v_mov_b32_e32 v159, 0x3e000000
	ds_write2_b32 v86, v90, v91 offset0:64 offset1:100
	ds_write2_b32 v86, v92, v93 offset0:136 offset1:172
	v_add_u32_e32 v82, 0xc00, v149
	s_mov_b64 s[10:11], -1
	s_and_b64 vcc, exec, s[16:17]
	v_lshl_add_u64 v[84:85], v[146:147], 1, s[14:15]
	v_lshlrev_b32_e32 v83, 1, v89
	v_lshlrev_b32_e32 v91, 3, v155
	ds_write2_b32 v82, v94, v95 offset0:96 offset1:132
	ds_write2_b32 v82, v96, v97 offset0:168 offset1:204
	s_cbranch_vccz .LBB11_3
	ds_read2_b32 v[92:93], v149 offset1:36
	ds_read2_b32 v[94:95], v149 offset0:72 offset1:108
	ds_read2_b32 v[96:97], v153 offset0:32 offset1:68
	ds_read2_b32 v[160:161], v153 offset0:104 offset1:140
	s_mov_b64 s[10:11], 0
	s_waitcnt vmcnt(8) lgkmcnt(3)
	v_add_f32_e32 v87, v152, v92
	v_cvt_f16_f32_e32 v87, v87
	v_mov_b32_e32 v92, v93
	s_waitcnt lgkmcnt(2)
	v_mov_b32_e32 v93, v94
	v_mov_b32_e32 v94, v95
	v_pk_add_f32 v[92:93], v[152:153], v[92:93] op_sel_hi:[0,1]
	s_waitcnt lgkmcnt(1)
	v_mov_b32_e32 v95, v96
	v_cvt_pk_f16_f32 v88, v92, v93
	v_pk_add_f32 v[94:95], v[152:153], v[94:95] op_sel_hi:[0,1]
	v_pack_b32_f16 v92, v87, v88
	v_cvt_pk_f16_f32 v87, v94, v95
	v_mov_b32_e32 v94, v97
	s_waitcnt lgkmcnt(0)
	v_mov_b32_e32 v95, v160
	v_alignbit_b32 v93, v87, v88, 16
	v_add_f32_e32 v88, v152, v161
	v_pk_add_f32 v[94:95], v[152:153], v[94:95] op_sel_hi:[0,1]
	v_cvt_f16_f32_e32 v88, v88
	v_cvt_pk_f16_f32 v90, v94, v95
	ds_read2_b32 v[160:161], v86 offset0:64 offset1:100
	v_alignbit_b32 v94, v90, v87, 16
	v_or3_b32 v87, v83, v91, v1
	v_lshlrev_b32_e32 v96, 4, v87
	ds_read2_b32 v[86:87], v86 offset0:136 offset1:172
	v_mov_b32_e32 v97, v147
	v_alignbit_b32 v95, v88, v90, 16
	v_lshl_add_u64 v[162:163], v[84:85], 0, v[96:97]
	global_store_dwordx4 v[162:163], v[92:95], off
	s_waitcnt lgkmcnt(1)
	v_add_f32_e32 v88, v152, v160
	ds_read2_b32 v[94:95], v82 offset0:96 offset1:132
	v_mov_b32_e32 v92, v161
	ds_read2_b32 v[160:161], v82 offset0:168 offset1:204
	v_cvt_f16_f32_e32 v88, v88
	s_waitcnt lgkmcnt(2)
	v_mov_b32_e32 v93, v86
	v_pk_add_f32 v[92:93], v[152:153], v[92:93] op_sel_hi:[0,1]
	v_cvt_pk_f16_f32 v90, v92, v93
	v_pack_b32_f16 v92, v88, v90
	v_mov_b32_e32 v86, v87
	s_waitcnt lgkmcnt(1)
	v_mov_b32_e32 v87, v94
	s_waitcnt lgkmcnt(0)
	v_add_f32_e32 v88, v152, v161
	v_pk_add_f32 v[86:87], v[152:153], v[86:87] op_sel_hi:[0,1]
	v_cvt_f16_f32_e32 v88, v88
	v_cvt_pk_f16_f32 v82, v86, v87
	v_mov_b32_e32 v86, v95
	v_mov_b32_e32 v87, v160
	v_pk_add_f32 v[86:87], v[152:153], v[86:87] op_sel_hi:[0,1]
	v_cvt_pk_f16_f32 v86, v86, v87
	v_alignbit_b32 v94, v86, v82, 16
	v_alignbit_b32 v95, v88, v86, 16
	v_or_b32_e32 v86, 0x800, v96
	v_mov_b32_e32 v87, v147
	v_alignbit_b32 v93, v82, v90, 16
	v_lshl_add_u64 v[86:87], v[84:85], 0, v[86:87]
	global_store_dwordx4 v[86:87], v[92:95], off

_Z6gemm_kILi1ELi128ELi4ELi8EEv5GArgs:
	v_lshlrev_b32_e32 v74, 4, v0
	s_getpc_b64 s[92:93]
	s_add_u32 s92, s92, 0xffff2af8
	s_addc_u32 s93, s93, 0xffffffff
	global_load_dword v75, v74, s[92:93]
	s_cmpk_lt_u32 s2, 0xc0
	s_mov_b64 s[4:5], -1
	s_cbranch_scc0 .LBB12_2
	s_load_dwordx4 s[4:7], s[0:1], 0x0
	v_lshrrev_b32_e32 v44, 6, v0
	s_lshl_b32 s3, s2, 7
	v_bfe_u32 v1, v0, 3, 3
	s_and_b32 s3, s3, 0xf80
	v_lshl_or_b32 v6, v44, 4, v1
	v_and_b32_e32 v2, 7, v0
	v_bitop3_b32 v4, v44, v2, 1 bitop3:0x6c
	v_or_b32_e32 v2, s3, v6
	v_mul_u32_u24_e32 v2, 0x340, v2
	v_bfe_u32 v5, v0, 4, 2
	v_lshlrev_b32_e32 v34, 1, v2
	v_mov_b32_e32 v35, 0
	v_xor_b32_e32 v5, v4, v5
	s_waitcnt lgkmcnt(0)
	v_lshl_add_u64 v[2:3], s[4:5], 0, v[34:35]
	v_lshlrev_b32_e32 v34, 4, v5
	v_or_b32_e32 v7, 8, v6
	v_lshl_add_u64 v[36:37], v[2:3], 0, v[34:35]
	v_or_b32_e32 v2, s3, v7
	v_bfe_u32 v5, v7, 1, 3
	s_lshl_b32 s8, s2, 2
	v_mul_u32_u24_e32 v2, 0x340, v2
	v_mov_b32_e32 v3, v35
	v_xor_b32_e32 v4, v4, v5
	v_lshl_add_u64 v[2:3], v[2:3], 1, s[4:5]
	v_lshlrev_b32_e32 v4, 4, v4
	v_mov_b32_e32 v5, v35
	s_and_b32 s10, s8, 0x380
	v_lshl_add_u64 v[38:39], v[2:3], 0, v[4:5]
	v_or_b32_e32 v2, s10, v6
	v_mul_u32_u24_e32 v2, 0x680, v2
	v_mov_b32_e32 v3, v35
	v_lshl_add_u64 v[2:3], s[6:7], 0, v[2:3]
	v_lshl_add_u64 v[40:41], v[2:3], 0, v[34:35]
	v_or_b32_e32 v2, s10, v7
	v_mul_u32_u24_e32 v34, 0x680, v2
	v_lshl_add_u64 v[2:3], s[6:7], 0, v[34:35]
	v_lshl_add_u64 v[42:43], v[2:3], 0, v[4:5]
	v_lshlrev_b32_e32 v4, 11, v44
	v_or_b32_e32 v2, 0x400, v4
	v_readfirstlane_b32 s19, v4
	s_mov_b32 m0, s19
	v_readfirstlane_b32 s20, v2
	v_or_b32_e32 v2, 0x10000, v4
	global_load_lds_dwordx4 v[36:37], off
	s_mov_b32 m0, s20
	v_readfirstlane_b32 s21, v2
	v_or_b32_e32 v2, 0x10400, v4
	global_load_lds_dwordx4 v[38:39], off
	s_mov_b32 m0, s21
	v_readfirstlane_b32 s22, v2
	v_or_b32_e32 v5, 0x4000, v4
	global_load_lds_dwordx4 v[40:41], off
	s_mov_b32 m0, s22
	s_mov_b64 s[4:5], 0x80
	v_readfirstlane_b32 s15, v5
	v_or_b32_e32 v5, 0x4400, v4
	global_load_lds_dwordx4 v[42:43], off
	v_lshl_add_u64 v[2:3], v[36:37], 0, s[4:5]
	s_mov_b32 m0, s15
	v_readfirstlane_b32 s16, v5
	v_or_b32_e32 v5, 0x14000, v4
	global_load_lds_dwordx4 v[2:3], off
	v_lshl_add_u64 v[2:3], v[38:39], 0, s[4:5]
	s_mov_b32 m0, s16
	v_readfirstlane_b32 s17, v5
	v_or_b32_e32 v5, 0x14400, v4
	global_load_lds_dwordx4 v[2:3], off
	v_lshl_add_u64 v[2:3], v[40:41], 0, s[4:5]
	s_mov_b32 m0, s17
	v_readfirstlane_b32 s18, v5
	v_or_b32_e32 v5, 0x8000, v4
	global_load_lds_dwordx4 v[2:3], off
	v_lshl_add_u64 v[2:3], v[42:43], 0, s[4:5]
	s_mov_b32 m0, s18
	s_mov_b64 s[4:5], 0x100
	v_readfirstlane_b32 s11, v5
	v_or_b32_e32 v5, 0x8400, v4
	global_load_lds_dwordx4 v[2:3], off
	v_lshl_add_u64 v[2:3], v[36:37], 0, s[4:5]
	s_mov_b32 m0, s11
	v_readfirstlane_b32 s12, v5
	v_or_b32_e32 v5, 0x18000, v4
	global_load_lds_dwordx4 v[2:3], off
	v_lshl_add_u64 v[2:3], v[38:39], 0, s[4:5]
	s_mov_b32 m0, s12
	v_readfirstlane_b32 s13, v5
	v_or_b32_e32 v5, 0x18400, v4
	global_load_lds_dwordx4 v[2:3], off
	v_lshl_add_u64 v[2:3], v[40:41], 0, s[4:5]
	s_mov_b32 m0, s13
	v_readfirstlane_b32 s14, v5
	v_or_b32_e32 v5, 0xc000, v4
	global_load_lds_dwordx4 v[2:3], off
	v_lshl_add_u64 v[2:3], v[42:43], 0, s[4:5]
	s_mov_b32 m0, s14
	s_mov_b64 s[4:5], 0x180
	v_readfirstlane_b32 s25, v5
	v_or_b32_e32 v5, 0xc400, v4
	global_load_lds_dwordx4 v[2:3], off
	v_lshl_add_u64 v[2:3], v[36:37], 0, s[4:5]
	s_mov_b32 m0, s25
	v_readfirstlane_b32 s23, v5
	v_or_b32_e32 v5, 0x1c000, v4
	s_waitcnt vmcnt(8)
	s_waitcnt vmcnt(0) lgkmcnt(0)
	s_barrier
	global_load_lds_dwordx4 v[2:3], off
	v_lshl_add_u64 v[2:3], v[38:39], 0, s[4:5]
	s_mov_b32 m0, s23
	v_readfirstlane_b32 s24, v5
	v_or_b32_e32 v4, 0x1c400, v4
	global_load_lds_dwordx4 v[2:3], off
	v_lshl_add_u64 v[2:3], v[40:41], 0, s[4:5]
	s_mov_b32 m0, s24
	v_readfirstlane_b32 s26, v4
	global_load_lds_dwordx4 v[2:3], off
	v_lshl_add_u64 v[2:3], v[42:43], 0, s[4:5]
	s_mov_b32 m0, s26
	v_bfe_u32 v46, v0, 5, 1
	global_load_lds_dwordx4 v[2:3], off
	v_lshrrev_b32_e32 v2, 1, v0
	v_bfe_u32 v3, v0, 4, 1
	v_bitop3_b32 v2, v2, v3, 7 bitop3:0x6c
	v_or_b32_e32 v3, 6, v46
	s_load_dwordx2 s[8:9], s[0:1], 0x18
	s_load_dwordx2 s[6:7], s[0:1], 0x30
	s_load_dwordx2 s[4:5], s[0:1], 0x48
	v_xor_b32_e32 v3, v2, v3
	v_lshlrev_b32_e32 v72, 4, v3
	v_or_b32_e32 v3, 4, v46
	v_xor_b32_e32 v3, v2, v3
	v_lshlrev_b32_e32 v62, 4, v3
	v_or_b32_e32 v3, 2, v46
	v_and_b32_e32 v47, 31, v0
	v_xor_b32_e32 v3, v2, v3
	v_xor_b32_e32 v2, v2, v46
	v_bfe_u32 v45, v0, 6, 2
	v_lshrrev_b32_e32 v34, 8, v0
	s_mov_b32 s27, 0x10000
	v_lshlrev_b32_e32 v50, 7, v47
	v_lshlrev_b32_e32 v6, 4, v2
	v_lshlrev_b32_e32 v2, 12, v45
	v_lshlrev_b32_e32 v68, 13, v34
	v_lshlrev_b32_e32 v52, 4, v3
	v_or3_b32 v73, v2, v50, s27
	v_or3_b32 v49, v6, v68, v50
	ds_read_b128 v[2:5], v49
	v_or_b32_e32 v51, v73, v6
	ds_read_b128 v[6:9], v51
	v_or_b32_e32 v14, v52, v68
	v_add_u32_e32 v48, v14, v50
	ds_read_b128 v[54:57], v48
	v_or_b32_e32 v53, v73, v52
	ds_read_b128 v[10:13], v49 offset:4096
	ds_read_b128 v[58:61], v53
	s_waitcnt lgkmcnt(0)
	v_mfma_f32_32x32x16_f16 v[18:33], v[2:5], v[6:9], 0
	v_or_b32_e32 v52, v62, v68
	v_add_u32_e32 v52, v52, v50
	v_mfma_f32_32x32x16_f16 v[18:33], v[54:57], v[58:61], v[18:33]
	ds_read_b128 v[54:57], v48 offset:4096
	v_mfma_f32_32x32x16_f16 v[2:17], v[10:13], v[6:9], 0
	s_waitcnt lgkmcnt(0)
	v_mfma_f32_32x32x16_f16 v[2:17], v[54:57], v[58:61], v[2:17]
	ds_read_b128 v[56:59], v52
	v_or_b32_e32 v54, v73, v62
	ds_read_b128 v[60:63], v54
	ds_read_b128 v[64:67], v52 offset:4096
	v_or_b32_e32 v55, v72, v68
	v_add_u32_e32 v50, v55, v50
	ds_read_b128 v[68:71], v50
	v_or_b32_e32 v55, v73, v72
	s_waitcnt lgkmcnt(0)
	v_mfma_f32_32x32x16_f16 v[18:33], v[56:59], v[60:63], v[18:33]
	ds_read_b128 v[56:59], v55
	v_mfma_f32_32x32x16_f16 v[2:17], v[64:67], v[60:63], v[2:17]
	ds_read_b128 v[60:63], v50 offset:4096
	s_waitcnt lgkmcnt(0)
	v_mfma_f32_32x32x16_f16 v[18:33], v[68:71], v[56:59], v[18:33]
	v_mfma_f32_32x32x16_f16 v[2:17], v[60:63], v[56:59], v[2:17]
	s_mov_b64 s[28:29], 0x200
	s_mov_b32 m0, s19
	v_lshl_add_u64 v[56:57], v[36:37], 0, s[28:29]
	s_waitcnt vmcnt(8)
	s_barrier
	global_load_lds_dwordx4 v[56:57], off
	v_lshl_add_u64 v[56:57], v[38:39], 0, s[28:29]
	s_mov_b32 m0, s20
	s_nop 0
	global_load_lds_dwordx4 v[56:57], off
	v_lshl_add_u64 v[56:57], v[40:41], 0, s[28:29]
	s_mov_b32 m0, s21
	s_nop 0
	global_load_lds_dwordx4 v[56:57], off
	v_lshl_add_u64 v[56:57], v[42:43], 0, s[28:29]
	s_mov_b32 m0, s22
	s_nop 0
	global_load_lds_dwordx4 v[56:57], off
	ds_read_b128 v[56:59], v49 offset:16384
	ds_read_b128 v[60:63], v51 offset:16384
	ds_read_b128 v[64:67], v49 offset:20480
	ds_read_b128 v[68:71], v48 offset:16384
	s_waitcnt lgkmcnt(0)
	v_mfma_f32_32x32x16_f16 v[18:33], v[56:59], v[60:63], v[18:33]
	ds_read_b128 v[56:59], v53 offset:16384
	v_mfma_f32_32x32x16_f16 v[2:17], v[64:67], v[60:63], v[2:17]
	ds_read_b128 v[60:63], v48 offset:20480
	s_waitcnt lgkmcnt(0)
	v_mfma_f32_32x32x16_f16 v[18:33], v[68:71], v[56:59], v[18:33]
	v_mfma_f32_32x32x16_f16 v[2:17], v[60:63], v[56:59], v[2:17]
	ds_read_b128 v[56:59], v52 offset:16384
	ds_read_b128 v[60:63], v54 offset:16384
	ds_read_b128 v[64:67], v52 offset:20480
	ds_read_b128 v[68:71], v50 offset:16384
	s_waitcnt lgkmcnt(0)
	v_mfma_f32_32x32x16_f16 v[18:33], v[56:59], v[60:63], v[18:33]
	ds_read_b128 v[56:59], v55 offset:16384
	v_mfma_f32_32x32x16_f16 v[2:17], v[64:67], v[60:63], v[2:17]
	ds_read_b128 v[60:63], v50 offset:20480
	s_waitcnt lgkmcnt(0)
	v_mfma_f32_32x32x16_f16 v[18:33], v[68:71], v[56:59], v[18:33]
	v_mfma_f32_32x32x16_f16 v[2:17], v[60:63], v[56:59], v[2:17]
	s_mov_b64 s[28:29], 0x280
	s_mov_b32 m0, s15
	v_lshl_add_u64 v[56:57], v[36:37], 0, s[28:29]
	s_waitcnt vmcnt(8)
	s_barrier
	global_load_lds_dwordx4 v[56:57], off
	v_lshl_add_u64 v[56:57], v[38:39], 0, s[28:29]
	s_mov_b32 m0, s16
	s_nop 0
	global_load_lds_dwordx4 v[56:57], off
	v_lshl_add_u64 v[56:57], v[40:41], 0, s[28:29]
	s_mov_b32 m0, s17
	s_nop 0
	global_load_lds_dwordx4 v[56:57], off
	v_lshl_add_u64 v[56:57], v[42:43], 0, s[28:29]
	s_mov_b32 m0, s18
	s_nop 0
	global_load_lds_dwordx4 v[56:57], off
	ds_read_b128 v[56:59], v49 offset:32768
	ds_read_b128 v[60:63], v51 offset:32768
	ds_read_b128 v[64:67], v49 offset:36864
	ds_read_b128 v[68:71], v48 offset:32768
	s_waitcnt lgkmcnt(0)
	v_mfma_f32_32x32x16_f16 v[18:33], v[56:59], v[60:63], v[18:33]
	ds_read_b128 v[56:59], v53 offset:32768
	v_mfma_f32_32x32x16_f16 v[2:17], v[64:67], v[60:63], v[2:17]
	ds_read_b128 v[60:63], v48 offset:36864
	s_waitcnt lgkmcnt(0)
	v_mfma_f32_32x32x16_f16 v[18:33], v[68:71], v[56:59], v[18:33]
	v_mfma_f32_32x32x16_f16 v[2:17], v[60:63], v[56:59], v[2:17]
	ds_read_b128 v[56:59], v52 offset:32768
	ds_read_b128 v[60:63], v54 offset:32768
	ds_read_b128 v[64:67], v52 offset:36864
	ds_read_b128 v[68:71], v50 offset:32768
	s_waitcnt lgkmcnt(0)
	v_mfma_f32_32x32x16_f16 v[18:33], v[56:59], v[60:63], v[18:33]
	ds_read_b128 v[56:59], v55 offset:32768
	v_mfma_f32_32x32x16_f16 v[2:17], v[64:67], v[60:63], v[2:17]
	ds_read_b128 v[60:63], v50 offset:36864
	s_waitcnt lgkmcnt(0)
	v_mfma_f32_32x32x16_f16 v[18:33], v[68:71], v[56:59], v[18:33]
	v_mfma_f32_32x32x16_f16 v[2:17], v[60:63], v[56:59], v[2:17]
	s_mov_b64 s[28:29], 0x300
	s_mov_b32 m0, s11
	v_lshl_add_u64 v[56:57], v[36:37], 0, s[28:29]
	s_waitcnt vmcnt(8)
	s_barrier
	global_load_lds_dwordx4 v[56:57], off
	v_lshl_add_u64 v[56:57], v[38:39], 0, s[28:29]
	s_mov_b32 m0, s12
	s_nop 0
	global_load_lds_dwordx4 v[56:57], off
	v_lshl_add_u64 v[56:57], v[40:41], 0, s[28:29]
	s_mov_b32 m0, s13
	s_nop 0
	global_load_lds_dwordx4 v[56:57], off
	v_lshl_add_u64 v[56:57], v[42:43], 0, s[28:29]
	s_mov_b32 m0, s14
	s_nop 0
	global_load_lds_dwordx4 v[56:57], off
	ds_read_b128 v[56:59], v49 offset:49152
	ds_read_b128 v[60:63], v51 offset:49152
	ds_read_b128 v[64:67], v49 offset:53248
	ds_read_b128 v[68:71], v48 offset:49152
	s_waitcnt lgkmcnt(0)
	v_mfma_f32_32x32x16_f16 v[18:33], v[56:59], v[60:63], v[18:33]
	ds_read_b128 v[56:59], v53 offset:49152
	v_mfma_f32_32x32x16_f16 v[2:17], v[64:67], v[60:63], v[2:17]
	ds_read_b128 v[60:63], v48 offset:53248
	s_waitcnt lgkmcnt(0)
	v_mfma_f32_32x32x16_f16 v[18:33], v[68:71], v[56:59], v[18:33]
	v_mfma_f32_32x32x16_f16 v[2:17], v[60:63], v[56:59], v[2:17]
	ds_read_b128 v[56:59], v52 offset:49152
	ds_read_b128 v[60:63], v54 offset:49152
	ds_read_b128 v[64:67], v52 offset:53248
	ds_read_b128 v[68:71], v50 offset:49152
	s_waitcnt lgkmcnt(0)
	v_mfma_f32_32x32x16_f16 v[18:33], v[56:59], v[60:63], v[18:33]
	ds_read_b128 v[56:59], v55 offset:49152
	v_mfma_f32_32x32x16_f16 v[2:17], v[64:67], v[60:63], v[2:17]
	ds_read_b128 v[60:63], v50 offset:53248
	s_waitcnt lgkmcnt(0)
	v_mfma_f32_32x32x16_f16 v[18:33], v[68:71], v[56:59], v[18:33]
	v_mfma_f32_32x32x16_f16 v[2:17], v[60:63], v[56:59], v[2:17]
	s_mov_b64 s[28:29], 0x380
	s_mov_b32 m0, s25
	v_lshl_add_u64 v[56:57], v[36:37], 0, s[28:29]
	s_waitcnt vmcnt(8)
	s_barrier
	global_load_lds_dwordx4 v[56:57], off
	v_lshl_add_u64 v[56:57], v[38:39], 0, s[28:29]
	s_mov_b32 m0, s23
	s_nop 0
	global_load_lds_dwordx4 v[56:57], off
	v_lshl_add_u64 v[56:57], v[40:41], 0, s[28:29]
	s_mov_b32 m0, s24
	s_nop 0
	global_load_lds_dwordx4 v[56:57], off
	v_lshl_add_u64 v[56:57], v[42:43], 0, s[28:29]
	s_mov_b32 m0, s26
	s_nop 0
	global_load_lds_dwordx4 v[56:57], off
	ds_read_b128 v[56:59], v49
	ds_read_b128 v[60:63], v51
	ds_read_b128 v[64:67], v49 offset:4096
	ds_read_b128 v[68:71], v48
	s_waitcnt lgkmcnt(0)
	v_mfma_f32_32x32x16_f16 v[18:33], v[56:59], v[60:63], v[18:33]
	ds_read_b128 v[56:59], v53
	v_mfma_f32_32x32x16_f16 v[2:17], v[64:67], v[60:63], v[2:17]
	ds_read_b128 v[60:63], v48 offset:4096
	s_waitcnt lgkmcnt(0)
	v_mfma_f32_32x32x16_f16 v[18:33], v[68:71], v[56:59], v[18:33]
	v_mfma_f32_32x32x16_f16 v[2:17], v[60:63], v[56:59], v[2:17]
	ds_read_b128 v[56:59], v52
	ds_read_b128 v[60:63], v54
	ds_read_b128 v[64:67], v52 offset:4096
	ds_read_b128 v[68:71], v50
	s_waitcnt lgkmcnt(0)
	v_mfma_f32_32x32x16_f16 v[18:33], v[56:59], v[60:63], v[18:33]
	ds_read_b128 v[56:59], v55
	v_mfma_f32_32x32x16_f16 v[2:17], v[64:67], v[60:63], v[2:17]
	ds_read_b128 v[60:63], v50 offset:4096
	s_waitcnt lgkmcnt(0)
	v_mfma_f32_32x32x16_f16 v[18:33], v[68:71], v[56:59], v[18:33]
	v_mfma_f32_32x32x16_f16 v[2:17], v[60:63], v[56:59], v[2:17]
	s_mov_b64 s[28:29], 0x400
	s_mov_b32 m0, s19
	v_lshl_add_u64 v[56:57], v[36:37], 0, s[28:29]
	s_waitcnt vmcnt(8)
	s_barrier
	global_load_lds_dwordx4 v[56:57], off
	v_lshl_add_u64 v[56:57], v[38:39], 0, s[28:29]
	s_mov_b32 m0, s20
	s_nop 0
	global_load_lds_dwordx4 v[56:57], off
	v_lshl_add_u64 v[56:57], v[40:41], 0, s[28:29]
	s_mov_b32 m0, s21
	s_nop 0
	global_load_lds_dwordx4 v[56:57], off
	v_lshl_add_u64 v[56:57], v[42:43], 0, s[28:29]
	s_mov_b32 m0, s22
	s_nop 0
	global_load_lds_dwordx4 v[56:57], off
	ds_read_b128 v[56:59], v49 offset:16384
	ds_read_b128 v[60:63], v51 offset:16384
	ds_read_b128 v[64:67], v49 offset:20480
	ds_read_b128 v[68:71], v48 offset:16384
	s_waitcnt lgkmcnt(0)
	v_mfma_f32_32x32x16_f16 v[18:33], v[56:59], v[60:63], v[18:33]
	ds_read_b128 v[56:59], v53 offset:16384
	v_mfma_f32_32x32x16_f16 v[2:17], v[64:67], v[60:63], v[2:17]
	ds_read_b128 v[60:63], v48 offset:20480
	s_waitcnt lgkmcnt(0)
	v_mfma_f32_32x32x16_f16 v[18:33], v[68:71], v[56:59], v[18:33]
	v_mfma_f32_32x32x16_f16 v[2:17], v[60:63], v[56:59], v[2:17]
	ds_read_b128 v[56:59], v52 offset:16384
	ds_read_b128 v[60:63], v54 offset:16384
	ds_read_b128 v[64:67], v52 offset:20480
	ds_read_b128 v[68:71], v50 offset:16384
	s_waitcnt lgkmcnt(0)
	v_mfma_f32_32x32x16_f16 v[18:33], v[56:59], v[60:63], v[18:33]
	ds_read_b128 v[56:59], v55 offset:16384
	v_mfma_f32_32x32x16_f16 v[2:17], v[64:67], v[60:63], v[2:17]
	ds_read_b128 v[60:63], v50 offset:20480
	s_waitcnt lgkmcnt(0)
	v_mfma_f32_32x32x16_f16 v[18:33], v[68:71], v[56:59], v[18:33]
	v_mfma_f32_32x32x16_f16 v[2:17], v[60:63], v[56:59], v[2:17]
	s_mov_b64 s[28:29], 0x480
	s_mov_b32 m0, s15
	v_lshl_add_u64 v[56:57], v[36:37], 0, s[28:29]
	s_waitcnt vmcnt(8)
	s_barrier
	global_load_lds_dwordx4 v[56:57], off
	v_lshl_add_u64 v[56:57], v[38:39], 0, s[28:29]
	s_mov_b32 m0, s16
	s_nop 0
	global_load_lds_dwordx4 v[56:57], off
	v_lshl_add_u64 v[56:57], v[40:41], 0, s[28:29]
	s_mov_b32 m0, s17
	s_nop 0
	global_load_lds_dwordx4 v[56:57], off
	v_lshl_add_u64 v[56:57], v[42:43], 0, s[28:29]
	s_mov_b32 m0, s18
	s_nop 0
	global_load_lds_dwordx4 v[56:57], off
	ds_read_b128 v[56:59], v49 offset:32768
	ds_read_b128 v[60:63], v51 offset:32768
	ds_read_b128 v[64:67], v49 offset:36864
	ds_read_b128 v[68:71], v48 offset:32768
	s_waitcnt lgkmcnt(0)
	v_mfma_f32_32x32x16_f16 v[18:33], v[56:59], v[60:63], v[18:33]
	ds_read_b128 v[56:59], v53 offset:32768
	v_mfma_f32_32x32x16_f16 v[2:17], v[64:67], v[60:63], v[2:17]
	ds_read_b128 v[60:63], v48 offset:36864
	s_waitcnt lgkmcnt(0)
	v_mfma_f32_32x32x16_f16 v[18:33], v[68:71], v[56:59], v[18:33]
	v_mfma_f32_32x32x16_f16 v[2:17], v[60:63], v[56:59], v[2:17]
	ds_read_b128 v[56:59], v52 offset:32768
	ds_read_b128 v[60:63], v54 offset:32768
	ds_read_b128 v[64:67], v52 offset:36864
	ds_read_b128 v[68:71], v50 offset:32768
	s_waitcnt lgkmcnt(0)
	v_mfma_f32_32x32x16_f16 v[18:33], v[56:59], v[60:63], v[18:33]
	ds_read_b128 v[56:59], v55 offset:32768
	v_mfma_f32_32x32x16_f16 v[2:17], v[64:67], v[60:63], v[2:17]
	ds_read_b128 v[60:63], v50 offset:36864
	s_waitcnt lgkmcnt(0)
	v_mfma_f32_32x32x16_f16 v[18:33], v[68:71], v[56:59], v[18:33]
	v_mfma_f32_32x32x16_f16 v[2:17], v[60:63], v[56:59], v[2:17]
	s_mov_b64 s[28:29], 0x500
	s_mov_b32 m0, s11
	v_lshl_add_u64 v[56:57], v[36:37], 0, s[28:29]
	s_waitcnt vmcnt(8)
	s_barrier
	global_load_lds_dwordx4 v[56:57], off
	v_lshl_add_u64 v[56:57], v[38:39], 0, s[28:29]
	s_mov_b32 m0, s12
	s_nop 0
	global_load_lds_dwordx4 v[56:57], off
	v_lshl_add_u64 v[56:57], v[40:41], 0, s[28:29]
	s_mov_b32 m0, s13
	s_nop 0
	global_load_lds_dwordx4 v[56:57], off
	v_lshl_add_u64 v[56:57], v[42:43], 0, s[28:29]
	s_mov_b32 m0, s14
	s_nop 0
	global_load_lds_dwordx4 v[56:57], off
	ds_read_b128 v[56:59], v49 offset:49152
	ds_read_b128 v[60:63], v51 offset:49152
	ds_read_b128 v[64:67], v49 offset:53248
	ds_read_b128 v[68:71], v48 offset:49152
	s_waitcnt lgkmcnt(0)
	v_mfma_f32_32x32x16_f16 v[18:33], v[56:59], v[60:63], v[18:33]
	ds_read_b128 v[56:59], v53 offset:49152
	v_mfma_f32_32x32x16_f16 v[2:17], v[64:67], v[60:63], v[2:17]
	ds_read_b128 v[60:63], v48 offset:53248
	s_waitcnt lgkmcnt(0)
	v_mfma_f32_32x32x16_f16 v[18:33], v[68:71], v[56:59], v[18:33]
	v_mfma_f32_32x32x16_f16 v[2:17], v[60:63], v[56:59], v[2:17]
	ds_read_b128 v[56:59], v52 offset:49152
	ds_read_b128 v[60:63], v54 offset:49152
	ds_read_b128 v[64:67], v52 offset:53248
	ds_read_b128 v[68:71], v50 offset:49152
	s_waitcnt lgkmcnt(0)
	v_mfma_f32_32x32x16_f16 v[18:33], v[56:59], v[60:63], v[18:33]
	ds_read_b128 v[56:59], v55 offset:49152
	v_mfma_f32_32x32x16_f16 v[2:17], v[64:67], v[60:63], v[2:17]
	ds_read_b128 v[60:63], v50 offset:53248
	s_waitcnt lgkmcnt(0)
	v_mfma_f32_32x32x16_f16 v[18:33], v[68:71], v[56:59], v[18:33]
	v_mfma_f32_32x32x16_f16 v[2:17], v[60:63], v[56:59], v[2:17]
	s_mov_b64 s[28:29], 0x580
	s_mov_b32 m0, s25
	v_lshl_add_u64 v[64:65], v[36:37], 0, s[28:29]
	s_waitcnt vmcnt(8)
	s_barrier
	global_load_lds_dwordx4 v[64:65], off
	v_lshl_add_u64 v[66:67], v[38:39], 0, s[28:29]
	s_mov_b32 m0, s23
	v_lshl_add_u64 v[68:69], v[40:41], 0, s[28:29]
	global_load_lds_dwordx4 v[66:67], off
	s_mov_b32 m0, s24
	v_lshl_add_u64 v[70:71], v[42:43], 0, s[28:29]
	global_load_lds_dwordx4 v[68:69], off
	s_mov_b32 m0, s26
	s_nop 0
	global_load_lds_dwordx4 v[70:71], off
	ds_read_b128 v[36:39], v49
	ds_read_b128 v[40:43], v51
	ds_read_b128 v[56:59], v49 offset:4096
	ds_read_b128 v[60:63], v48
	s_waitcnt lgkmcnt(0)
	v_mfma_f32_32x32x16_f16 v[18:33], v[36:39], v[40:43], v[18:33]
	ds_read_b128 v[36:39], v53
	v_mfma_f32_32x32x16_f16 v[2:17], v[56:59], v[40:43], v[2:17]
	ds_read_b128 v[40:43], v48 offset:4096
	s_waitcnt lgkmcnt(0)
	v_mfma_f32_32x32x16_f16 v[18:33], v[60:63], v[36:39], v[18:33]
	v_mfma_f32_32x32x16_f16 v[2:17], v[40:43], v[36:39], v[2:17]
	ds_read_b128 v[36:39], v52
	ds_read_b128 v[40:43], v54
	ds_read_b128 v[56:59], v52 offset:4096
	ds_read_b128 v[60:63], v50
	s_waitcnt lgkmcnt(0)
	v_mfma_f32_32x32x16_f16 v[18:33], v[36:39], v[40:43], v[18:33]
	ds_read_b128 v[36:39], v55
	v_mfma_f32_32x32x16_f16 v[2:17], v[56:59], v[40:43], v[2:17]
	ds_read_b128 v[40:43], v50 offset:4096
	s_waitcnt lgkmcnt(0)
	v_mfma_f32_32x32x16_f16 v[18:33], v[60:63], v[36:39], v[18:33]
	v_mfma_f32_32x32x16_f16 v[2:17], v[40:43], v[36:39], v[2:17]
	s_mov_b32 m0, s19
	s_waitcnt vmcnt(8)
	s_barrier
	global_load_lds_dwordx4 v[64:65], off
	s_mov_b32 m0, s20
	s_nop 0
	global_load_lds_dwordx4 v[66:67], off
	s_mov_b32 m0, s21
	s_nop 0
	global_load_lds_dwordx4 v[68:69], off
	s_mov_b32 m0, s22
	s_nop 0
	global_load_lds_dwordx4 v[70:71], off
	ds_read_b128 v[36:39], v49 offset:16384
	ds_read_b128 v[40:43], v51 offset:16384
	ds_read_b128 v[56:59], v49 offset:20480
	ds_read_b128 v[60:63], v48 offset:16384
	s_waitcnt lgkmcnt(0)
	v_mfma_f32_32x32x16_f16 v[18:33], v[36:39], v[40:43], v[18:33]
	ds_read_b128 v[36:39], v53 offset:16384
	v_mfma_f32_32x32x16_f16 v[2:17], v[56:59], v[40:43], v[2:17]
	ds_read_b128 v[40:43], v48 offset:20480
	s_waitcnt lgkmcnt(0)
	v_mfma_f32_32x32x16_f16 v[18:33], v[60:63], v[36:39], v[18:33]
	v_mfma_f32_32x32x16_f16 v[2:17], v[40:43], v[36:39], v[2:17]
	ds_read_b128 v[36:39], v52 offset:16384
	ds_read_b128 v[40:43], v54 offset:16384
	ds_read_b128 v[56:59], v52 offset:20480
	ds_read_b128 v[60:63], v50 offset:16384
	s_waitcnt lgkmcnt(0)
	v_mfma_f32_32x32x16_f16 v[18:33], v[36:39], v[40:43], v[18:33]
	ds_read_b128 v[36:39], v55 offset:16384
	v_mfma_f32_32x32x16_f16 v[2:17], v[56:59], v[40:43], v[2:17]
	ds_read_b128 v[40:43], v50 offset:20480
	s_waitcnt lgkmcnt(0)
	v_mfma_f32_32x32x16_f16 v[18:33], v[60:63], v[36:39], v[18:33]
	v_mfma_f32_32x32x16_f16 v[2:17], v[40:43], v[36:39], v[2:17]
	s_mov_b32 m0, s15
	s_waitcnt vmcnt(8)
	s_barrier
	global_load_lds_dwordx4 v[64:65], off
	s_mov_b32 m0, s16
	s_nop 0
	global_load_lds_dwordx4 v[66:67], off
	s_mov_b32 m0, s17
	s_nop 0
	global_load_lds_dwordx4 v[68:69], off
	s_mov_b32 m0, s18
	s_nop 0
	global_load_lds_dwordx4 v[70:71], off
	ds_read_b128 v[36:39], v49 offset:32768
	ds_read_b128 v[40:43], v51 offset:32768
	ds_read_b128 v[56:59], v49 offset:36864
	ds_read_b128 v[60:63], v48 offset:32768
	s_waitcnt lgkmcnt(0)
	v_mfma_f32_32x32x16_f16 v[18:33], v[36:39], v[40:43], v[18:33]
	ds_read_b128 v[36:39], v53 offset:32768
	v_mfma_f32_32x32x16_f16 v[2:17], v[56:59], v[40:43], v[2:17]
	ds_read_b128 v[40:43], v48 offset:36864
	s_waitcnt lgkmcnt(0)
	v_mfma_f32_32x32x16_f16 v[18:33], v[60:63], v[36:39], v[18:33]
	v_mfma_f32_32x32x16_f16 v[2:17], v[40:43], v[36:39], v[2:17]
	ds_read_b128 v[36:39], v52 offset:32768
	ds_read_b128 v[40:43], v54 offset:32768
	ds_read_b128 v[56:59], v52 offset:36864
	ds_read_b128 v[60:63], v50 offset:32768
	s_waitcnt lgkmcnt(0)
	v_mfma_f32_32x32x16_f16 v[18:33], v[36:39], v[40:43], v[18:33]
	ds_read_b128 v[36:39], v55 offset:32768
	v_mfma_f32_32x32x16_f16 v[2:17], v[56:59], v[40:43], v[2:17]
	ds_read_b128 v[40:43], v50 offset:36864
	s_waitcnt lgkmcnt(0)
	v_mfma_f32_32x32x16_f16 v[18:33], v[60:63], v[36:39], v[18:33]
	v_mfma_f32_32x32x16_f16 v[2:17], v[40:43], v[36:39], v[2:17]
	s_mov_b32 m0, s11
	s_waitcnt vmcnt(8)
	s_barrier
	global_load_lds_dwordx4 v[64:65], off
	s_mov_b32 m0, s12
	s_nop 0
	global_load_lds_dwordx4 v[66:67], off
	s_mov_b32 m0, s13
	s_nop 0
	global_load_lds_dwordx4 v[68:69], off
	s_mov_b32 m0, s14
	s_nop 0
	global_load_lds_dwordx4 v[70:71], off
	ds_read_b128 v[36:39], v49 offset:49152
	ds_read_b128 v[40:43], v51 offset:49152
	ds_read_b128 v[56:59], v49 offset:53248
	ds_read_b128 v[60:63], v48 offset:49152
	s_waitcnt lgkmcnt(0)
	v_mfma_f32_32x32x16_f16 v[18:33], v[36:39], v[40:43], v[18:33]
	ds_read_b128 v[36:39], v53 offset:49152
	v_mfma_f32_32x32x16_f16 v[2:17], v[56:59], v[40:43], v[2:17]
	ds_read_b128 v[40:43], v48 offset:53248
	s_waitcnt lgkmcnt(0)
	v_mfma_f32_32x32x16_f16 v[18:33], v[60:63], v[36:39], v[18:33]
	v_mfma_f32_32x32x16_f16 v[2:17], v[40:43], v[36:39], v[2:17]
	ds_read_b128 v[36:39], v52 offset:49152
	ds_read_b128 v[40:43], v54 offset:49152
	ds_read_b128 v[56:59], v52 offset:53248
	ds_read_b128 v[60:63], v50 offset:49152
	s_waitcnt lgkmcnt(0)
	v_mfma_f32_32x32x16_f16 v[18:33], v[36:39], v[40:43], v[18:33]
	ds_read_b128 v[36:39], v55 offset:49152
	v_mfma_f32_32x32x16_f16 v[2:17], v[56:59], v[40:43], v[2:17]
	ds_read_b128 v[40:43], v50 offset:53248
	s_waitcnt lgkmcnt(0)
	v_mfma_f32_32x32x16_f16 v[18:33], v[60:63], v[36:39], v[18:33]
	v_mfma_f32_32x32x16_f16 v[2:17], v[40:43], v[36:39], v[2:17]
	v_mul_u32_u24_e32 v56, 0x2400, v44
	v_lshl_or_b32 v36, v47, 2, v56
	s_movk_i32 s11, 0x240
	v_mad_u32_u24 v36, v46, s11, v36
	s_waitcnt vmcnt(8)
	s_barrier
	s_waitcnt vmcnt(0)
	s_waitcnt vmcnt(0)
	s_barrier
	s_nop 3
	ds_write2_b32 v36, v18, v19 offset1:36
	ds_write2_b32 v36, v20, v21 offset0:72 offset1:108
	v_add_u32_e32 v18, 0x400, v36
	ds_write2_b32 v18, v22, v23 offset0:32 offset1:68
	ds_write2_b32 v18, v24, v25 offset0:104 offset1:140
	v_add_u32_e32 v18, 0x800, v36
	ds_write2_b32 v18, v26, v27 offset0:64 offset1:100
	ds_write2_b32 v18, v28, v29 offset0:136 offset1:172
	v_add_u32_e32 v18, 0xc00, v36
	ds_write2_b32 v18, v30, v31 offset0:96 offset1:132
	ds_write2_b32 v18, v32, v33 offset0:168 offset1:204
	v_add_u32_e32 v18, 0x1000, v36
	ds_write2_b32 v18, v2, v3 offset0:128 offset1:164
	ds_write2_b32 v18, v4, v5 offset0:200 offset1:236
	v_add_u32_e32 v2, 0x1400, v36
	ds_write2_b32 v2, v6, v7 offset0:160 offset1:196
	v_add_u32_e32 v2, 0x1600, v36
	ds_write2_b32 v2, v8, v9 offset0:104 offset1:140
	v_add_u32_e32 v2, 0x1800, v36
	ds_write2_b32 v2, v10, v11 offset0:192 offset1:228
	v_add_u32_e32 v2, 0x1c00, v36
	ds_write2_b32 v2, v12, v13 offset0:8 offset1:44
	v_add_u32_e32 v2, 0x1e00, v36
	v_lshl_or_b32 v5, v45, 5, s10
	v_lshlrev_b32_e32 v6, 2, v0
	ds_write2_b32 v2, v14, v15 offset0:96 offset1:132
	v_add_u32_e32 v2, 0x2000, v36
	v_lshlrev_b32_e32 v4, 6, v34
	v_lshlrev_b32_e32 v34, 2, v5
	v_and_b32_e32 v6, 28, v6
	ds_write2_b32 v2, v16, v17 offset0:40 offset1:76
	v_lshl_add_u64 v[2:3], s[8:9], 0, v[34:35]
	v_lshlrev_b32_e32 v34, 2, v6
	v_lshl_add_u64 v[10:11], v[2:3], 0, v[34:35]
	v_or3_b32 v2, s3, v4, v1
	v_or_b32_e32 v3, v5, v6
	s_movk_i32 s3, 0x300
	v_mad_u32_u24 v36, v2, s3, v3
	v_add_u32_e32 v2, 0x4800, v36
	v_mov_b32_e32 v3, v35
	v_lshlrev_b64 v[40:41], 2, v[2:3]
	v_lshl_add_u64 v[12:13], s[6:7], 0, v[40:41]
	global_load_dwordx4 v[2:5], v[10:11], off
	global_load_dwordx4 v[6:9], v[12:13], off
	v_add_u32_e32 v10, 0x3000, v36
	v_mov_b32_e32 v11, v35
	v_lshlrev_b64 v[42:43], 2, v[10:11]
	v_lshl_add_u64 v[10:11], s[6:7], 0, v[42:43]
	global_load_dwordx4 v[10:13], v[10:11], off
	v_add_u32_e32 v14, 0x1800, v36
	v_mov_b32_e32 v15, v35
	v_lshlrev_b64 v[44:45], 2, v[14:15]
	v_lshl_add_u64 v[14:15], s[6:7], 0, v[44:45]
	v_mov_b32_e32 v37, v35
	global_load_dwordx4 v[14:17], v[14:15], off
	v_lshlrev_b64 v[46:47], 2, v[36:37]
	v_lshl_add_u64 v[18:19], s[6:7], 0, v[46:47]
	global_load_dwordx4 v[18:21], v[18:19], off
	v_add_u32_e32 v22, 0x6000, v36
	v_mov_b32_e32 v23, v35
	v_lshlrev_b64 v[48:49], 2, v[22:23]
	v_lshl_add_u64 v[22:23], s[6:7], 0, v[48:49]
	v_add_u32_e32 v26, 0x7800, v36
	v_mov_b32_e32 v27, v35
	global_load_dwordx4 v[22:25], v[22:23], off
	v_lshlrev_b64 v[50:51], 2, v[26:27]
	v_lshl_add_u64 v[26:27], s[6:7], 0, v[50:51]
	global_load_dwordx4 v[26:29], v[26:27], off
	v_add_u32_e32 v30, 0x9000, v36
	v_mov_b32_e32 v31, v35
	v_add_u32_e32 v36, 0xa800, v36
	v_lshlrev_b64 v[52:53], 2, v[30:31]
	v_lshlrev_b64 v[54:55], 2, v[36:37]
	v_lshl_add_u64 v[30:31], s[6:7], 0, v[52:53]
	v_lshl_add_u64 v[36:37], s[6:7], 0, v[54:55]
	global_load_dwordx4 v[30:33], v[30:31], off
	v_or_b32_e32 v34, v56, v34
	global_load_dwordx4 v[36:39], v[36:37], off
	s_movk_i32 s3, 0x90
	v_mad_u32_u24 v1, v1, s3, v34
	v_lshl_add_u64 v[58:59], s[4:5], 0, v[42:43]
	v_lshl_add_u64 v[60:61], s[4:5], 0, v[40:41]
	ds_read_b128 v[40:43], v1 offset:3456
	v_lshl_add_u64 v[34:35], s[4:5], 0, v[46:47]
	v_lshl_add_u64 v[56:57], s[4:5], 0, v[44:45]
	ds_read_b128 v[44:47], v1 offset:2304
	v_lshl_add_u64 v[48:49], s[4:5], 0, v[48:49]
	v_lshl_add_u64 v[50:51], s[4:5], 0, v[50:51]
	v_lshl_add_u64 v[52:53], s[4:5], 0, v[52:53]
	v_lshl_add_u64 v[54:55], s[4:5], 0, v[54:55]
	s_mov_b64 s[4:5], 0
	s_waitcnt vmcnt(8) lgkmcnt(1)
	v_pk_add_f32 v[40:41], v[2:3], v[40:41]
	s_waitcnt vmcnt(7)
	v_pk_add_f32 v[6:7], v[40:41], v[6:7]
	v_pk_add_f32 v[40:41], v[4:5], v[42:43]
	s_waitcnt lgkmcnt(0)
	v_pk_add_f32 v[44:45], v[2:3], v[44:45]
	v_pk_add_f32 v[8:9], v[40:41], v[8:9]
	ds_read_b128 v[40:43], v1 offset:1152
	s_waitcnt vmcnt(6)
	v_pk_add_f32 v[10:11], v[44:45], v[10:11]
	v_pk_add_f32 v[44:45], v[4:5], v[46:47]
	s_nop 0
	v_pk_add_f32 v[12:13], v[44:45], v[12:13]
	ds_read_b128 v[44:47], v1
	s_waitcnt lgkmcnt(1)
	v_pk_add_f32 v[40:41], v[2:3], v[40:41]
	s_waitcnt vmcnt(5)
	v_pk_add_f32 v[14:15], v[40:41], v[14:15]
	v_pk_add_f32 v[40:41], v[4:5], v[42:43]
	s_nop 0
	v_pk_add_f32 v[16:17], v[40:41], v[16:17]
	s_waitcnt lgkmcnt(0)
	v_pk_add_f32 v[40:41], v[2:3], v[44:45]
	s_waitcnt vmcnt(4)
	v_pk_add_f32 v[18:19], v[40:41], v[18:19]
	v_pk_add_f32 v[40:41], v[4:5], v[46:47]
	s_nop 0
	v_pk_add_f32 v[20:21], v[40:41], v[20:21]
	global_store_dwordx4 v[34:35], v[18:21], off
	ds_read_b128 v[18:21], v1 offset:4608
	global_store_dwordx4 v[56:57], v[14:17], off
	global_store_dwordx4 v[58:59], v[10:13], off
	global_store_dwordx4 v[60:61], v[6:9], off
	ds_read_b128 v[6:9], v1 offset:5760
	s_waitcnt lgkmcnt(1)
	v_pk_add_f32 v[10:11], v[2:3], v[18:19]
	v_pk_add_f32 v[12:13], v[4:5], v[20:21]
	s_waitcnt vmcnt(7)
	v_pk_add_f32 v[10:11], v[10:11], v[22:23]
	v_pk_add_f32 v[12:13], v[12:13], v[24:25]
	global_store_dwordx4 v[48:49], v[10:13], off
	ds_read_b128 v[10:13], v1 offset:6912
	s_waitcnt lgkmcnt(1)
	v_pk_add_f32 v[6:7], v[2:3], v[6:7]
	v_pk_add_f32 v[8:9], v[4:5], v[8:9]
	s_waitcnt vmcnt(7)
	v_pk_add_f32 v[6:7], v[6:7], v[26:27]
	v_pk_add_f32 v[8:9], v[8:9], v[28:29]
	global_store_dwordx4 v[50:51], v[6:9], off
	ds_read_b128 v[6:9], v1 offset:8064
	s_waitcnt lgkmcnt(1)
	v_pk_add_f32 v[10:11], v[2:3], v[10:11]
	v_pk_add_f32 v[12:13], v[4:5], v[12:13]
	s_waitcnt vmcnt(7)
	v_pk_add_f32 v[10:11], v[10:11], v[30:31]
	v_pk_add_f32 v[12:13], v[12:13], v[32:33]
	s_waitcnt lgkmcnt(0)
	v_pk_add_f32 v[2:3], v[2:3], v[6:7]
	v_pk_add_f32 v[4:5], v[4:5], v[8:9]
	s_waitcnt vmcnt(6)
	v_pk_add_f32 v[2:3], v[2:3], v[36:37]
	v_pk_add_f32 v[4:5], v[4:5], v[38:39]
	global_store_dwordx4 v[52:53], v[10:13], off
	global_store_dwordx4 v[54:55], v[2:5], off
